# phase 7: hand-written FFN-norm part (x1 = x + y, RMS, h, hi/lo split, fp8 copy): chunk vectors g/sc/sh loaded once for 4 rows and prefetched one chunk ahead; same arithmetic
# speedup vs baseline: 1.0123x; 1.0030x over previous
.LBB0_883:
	s_lshl_b32 s58, s57, 5
	s_waitcnt lgkmcnt(0)
	v_add_u32_e32 v44, s58, v129
	v_lshlrev_b32_e32 v45, 2, v128
	v_lshl_add_u32 v222, v44, 13, v45
	v_add_u32_e32 v44, 1, v44
	v_lshl_add_u32 v223, v44, 13, v45
	v_add_u32_e32 v44, 1, v44
	v_lshl_add_u32 v224, v44, 13, v45
	v_add_u32_e32 v44, 1, v44
	v_lshl_add_u32 v225, v44, 13, v45
	v_add_u32_e32 v44, s58, v129
	v_lshlrev_b32_e32 v45, 1, v128
	v_lshl_add_u32 v226, v44, 12, v45
	v_add_u32_e32 v44, 1, v44
	v_lshl_add_u32 v227, v44, 12, v45
	v_add_u32_e32 v44, 1, v44
	v_lshl_add_u32 v228, v44, 12, v45
	v_add_u32_e32 v44, 1, v44
	v_lshl_add_u32 v229, v44, 12, v45
	v_add_u32_e32 v44, s58, v129
	v_lshl_add_u32 v230, v44, 11, v128
	v_add_u32_e32 v44, 1, v44
	v_lshl_add_u32 v231, v44, 11, v128
	v_add_u32_e32 v44, 1, v44
	v_lshl_add_u32 v0, v44, 11, v128
	v_add_u32_e32 v44, 1, v44
	v_lshl_add_u32 v3, v44, 11, v128
	s_add_u32 s98, s26, 0x1000
	s_addc_u32 s99, s27, 0
	global_load_dwordx4 v[4:7], v222, s[26:27] offset:0 nt
	global_load_dwordx2 v[158:159], v226, s[22:23] offset:0 nt
	global_load_dwordx4 v[8:11], v222, s[26:27] offset:1024 nt
	global_load_dwordx2 v[160:161], v226, s[22:23] offset:512 nt
	global_load_dwordx4 v[12:15], v222, s[26:27] offset:2048 nt
	global_load_dwordx2 v[162:163], v226, s[22:23] offset:1024 nt
	global_load_dwordx4 v[16:19], v222, s[26:27] offset:3072 nt
	global_load_dwordx2 v[164:165], v226, s[22:23] offset:1536 nt
	global_load_dwordx4 v[46:49], v222, s[98:99] offset:0 nt
	global_load_dwordx2 v[166:167], v226, s[22:23] offset:2048 nt
	global_load_dwordx4 v[50:53], v222, s[98:99] offset:1024 nt
	global_load_dwordx2 v[168:169], v226, s[22:23] offset:2560 nt
	global_load_dwordx4 v[54:57], v222, s[98:99] offset:2048 nt
	global_load_dwordx2 v[170:171], v226, s[22:23] offset:3072 nt
	global_load_dwordx4 v[58:61], v222, s[98:99] offset:3072 nt
	global_load_dwordx2 v[172:173], v226, s[22:23] offset:3584 nt
	global_load_dwordx4 v[20:23], v223, s[26:27] offset:0 nt
	global_load_dwordx2 v[174:175], v227, s[22:23] offset:0 nt
	global_load_dwordx4 v[24:27], v223, s[26:27] offset:1024 nt
	global_load_dwordx2 v[176:177], v227, s[22:23] offset:512 nt
	global_load_dwordx4 v[28:31], v223, s[26:27] offset:2048 nt
	global_load_dwordx2 v[178:179], v227, s[22:23] offset:1024 nt
	global_load_dwordx4 v[32:35], v223, s[26:27] offset:3072 nt
	global_load_dwordx2 v[180:181], v227, s[22:23] offset:1536 nt
	global_load_dwordx4 v[62:65], v223, s[98:99] offset:0 nt
	global_load_dwordx2 v[182:183], v227, s[22:23] offset:2048 nt
	global_load_dwordx4 v[66:69], v223, s[98:99] offset:1024 nt
	global_load_dwordx2 v[184:185], v227, s[22:23] offset:2560 nt
	global_load_dwordx4 v[70:73], v223, s[98:99] offset:2048 nt
	global_load_dwordx2 v[186:187], v227, s[22:23] offset:3072 nt
	global_load_dwordx4 v[74:77], v223, s[98:99] offset:3072 nt
	global_load_dwordx2 v[188:189], v227, s[22:23] offset:3584 nt
	global_load_dwordx4 v[36:39], v224, s[26:27] offset:0 nt
	global_load_dwordx2 v[190:191], v228, s[22:23] offset:0 nt
	global_load_dwordx4 v[40:43], v224, s[26:27] offset:1024 nt
	global_load_dwordx2 v[192:193], v228, s[22:23] offset:512 nt
	global_load_dwordx4 v[110:113], v224, s[26:27] offset:2048 nt
	global_load_dwordx2 v[194:195], v228, s[22:23] offset:1024 nt
	global_load_dwordx4 v[114:117], v224, s[26:27] offset:3072 nt
	global_load_dwordx2 v[196:197], v228, s[22:23] offset:1536 nt
	global_load_dwordx4 v[78:81], v224, s[98:99] offset:0 nt
	global_load_dwordx2 v[198:199], v228, s[22:23] offset:2048 nt
	global_load_dwordx4 v[82:85], v224, s[98:99] offset:1024 nt
	global_load_dwordx2 v[200:201], v228, s[22:23] offset:2560 nt
	global_load_dwordx4 v[86:89], v224, s[98:99] offset:2048 nt
	global_load_dwordx2 v[202:203], v228, s[22:23] offset:3072 nt
	global_load_dwordx4 v[90:93], v224, s[98:99] offset:3072 nt
	global_load_dwordx2 v[204:205], v228, s[22:23] offset:3584 nt
	global_load_dwordx4 v[118:121], v225, s[26:27] offset:0 nt
	global_load_dwordx2 v[206:207], v229, s[22:23] offset:0 nt
	global_load_dwordx4 v[122:125], v225, s[26:27] offset:1024 nt
	global_load_dwordx2 v[208:209], v229, s[22:23] offset:512 nt
	global_load_dwordx4 v[150:153], v225, s[26:27] offset:2048 nt
	global_load_dwordx2 v[210:211], v229, s[22:23] offset:1024 nt
	global_load_dwordx4 v[154:157], v225, s[26:27] offset:3072 nt
	global_load_dwordx2 v[212:213], v229, s[22:23] offset:1536 nt
	global_load_dwordx4 v[94:97], v225, s[98:99] offset:0 nt
	global_load_dwordx2 v[214:215], v229, s[22:23] offset:2048 nt
	global_load_dwordx4 v[98:101], v225, s[98:99] offset:1024 nt
	global_load_dwordx2 v[216:217], v229, s[22:23] offset:2560 nt
	s_waitcnt vmcnt(59)
	global_load_dwordx4 v[102:105], v225, s[98:99] offset:2048 nt
	s_waitcnt vmcnt(59)
	global_load_dwordx2 v[218:219], v229, s[22:23] offset:3072 nt
	s_waitcnt vmcnt(59)
	global_load_dwordx4 v[106:109], v225, s[98:99] offset:3072 nt
	s_waitcnt vmcnt(59)
	global_load_dwordx2 v[220:221], v229, s[22:23] offset:3584 nt
	v_lshlrev_b32_e32 v44, 16, v158
	v_and_b32_e32 v45, 0xffff0000, v158
	v_lshlrev_b32_e32 v158, 16, v159
	v_and_b32_e32 v159, 0xffff0000, v159
	v_pk_add_f32 v[4:5], v[4:5], v[44:45]
	v_pk_add_f32 v[6:7], v[6:7], v[158:159]
	v_cvt_pk_bf16_f32 v158, v4, v5
	v_cvt_pk_bf16_f32 v159, v6, v7
	s_waitcnt vmcnt(59)
	global_store_dwordx2 v226, v[158:159], s[22:23] offset:0
	v_mul_f32_e32 v126, v4, v4
	v_fmac_f32_e32 v126, v5, v5
	v_fmac_f32_e32 v126, v6, v6
	v_fmac_f32_e32 v126, v7, v7
	v_lshlrev_b32_e32 v44, 16, v160
	v_and_b32_e32 v45, 0xffff0000, v160
	v_lshlrev_b32_e32 v160, 16, v161
	v_and_b32_e32 v161, 0xffff0000, v161
	v_pk_add_f32 v[8:9], v[8:9], v[44:45]
	v_pk_add_f32 v[10:11], v[10:11], v[160:161]
	v_cvt_pk_bf16_f32 v160, v8, v9
	v_cvt_pk_bf16_f32 v161, v10, v11
	s_waitcnt vmcnt(59)
	global_store_dwordx2 v226, v[160:161], s[22:23] offset:512
	v_fmac_f32_e32 v126, v8, v8
	v_fmac_f32_e32 v126, v9, v9
	v_fmac_f32_e32 v126, v10, v10
	v_fmac_f32_e32 v126, v11, v11
	v_lshlrev_b32_e32 v44, 16, v162
	v_and_b32_e32 v45, 0xffff0000, v162
	v_lshlrev_b32_e32 v162, 16, v163
	v_and_b32_e32 v163, 0xffff0000, v163
	v_pk_add_f32 v[12:13], v[12:13], v[44:45]
	v_pk_add_f32 v[14:15], v[14:15], v[162:163]
	v_cvt_pk_bf16_f32 v162, v12, v13
	v_cvt_pk_bf16_f32 v163, v14, v15
	s_waitcnt vmcnt(59)
	global_store_dwordx2 v226, v[162:163], s[22:23] offset:1024
	v_fmac_f32_e32 v126, v12, v12
	v_fmac_f32_e32 v126, v13, v13
	v_fmac_f32_e32 v126, v14, v14
	v_fmac_f32_e32 v126, v15, v15
	s_waitcnt vmcnt(59)
	v_lshlrev_b32_e32 v44, 16, v164
	v_and_b32_e32 v45, 0xffff0000, v164
	v_lshlrev_b32_e32 v164, 16, v165
	v_and_b32_e32 v165, 0xffff0000, v165
	v_pk_add_f32 v[16:17], v[16:17], v[44:45]
	v_pk_add_f32 v[18:19], v[18:19], v[164:165]
	v_cvt_pk_bf16_f32 v164, v16, v17
	v_cvt_pk_bf16_f32 v165, v18, v19
	global_store_dwordx2 v226, v[164:165], s[22:23] offset:1536
	v_fmac_f32_e32 v126, v16, v16
	v_fmac_f32_e32 v126, v17, v17
	v_fmac_f32_e32 v126, v18, v18
	v_fmac_f32_e32 v126, v19, v19
	s_waitcnt vmcnt(58)
	v_lshlrev_b32_e32 v44, 16, v166
	v_and_b32_e32 v45, 0xffff0000, v166
	v_lshlrev_b32_e32 v166, 16, v167
	v_and_b32_e32 v167, 0xffff0000, v167
	v_pk_add_f32 v[46:47], v[46:47], v[44:45]
	v_pk_add_f32 v[48:49], v[48:49], v[166:167]
	v_cvt_pk_bf16_f32 v166, v46, v47
	v_cvt_pk_bf16_f32 v167, v48, v49
	global_store_dwordx2 v226, v[166:167], s[22:23] offset:2048
	v_fmac_f32_e32 v126, v46, v46
	v_fmac_f32_e32 v126, v47, v47
	v_fmac_f32_e32 v126, v48, v48
	v_fmac_f32_e32 v126, v49, v49
	s_waitcnt vmcnt(57)
	v_lshlrev_b32_e32 v44, 16, v168
	v_and_b32_e32 v45, 0xffff0000, v168
	v_lshlrev_b32_e32 v168, 16, v169
	v_and_b32_e32 v169, 0xffff0000, v169
	v_pk_add_f32 v[50:51], v[50:51], v[44:45]
	v_pk_add_f32 v[52:53], v[52:53], v[168:169]
	v_cvt_pk_bf16_f32 v168, v50, v51
	v_cvt_pk_bf16_f32 v169, v52, v53
	global_store_dwordx2 v226, v[168:169], s[22:23] offset:2560
	v_fmac_f32_e32 v126, v50, v50
	v_fmac_f32_e32 v126, v51, v51
	v_fmac_f32_e32 v126, v52, v52
	v_fmac_f32_e32 v126, v53, v53
	s_waitcnt vmcnt(56)
	v_lshlrev_b32_e32 v44, 16, v170
	v_and_b32_e32 v45, 0xffff0000, v170
	v_lshlrev_b32_e32 v170, 16, v171
	v_and_b32_e32 v171, 0xffff0000, v171
	v_pk_add_f32 v[54:55], v[54:55], v[44:45]
	v_pk_add_f32 v[56:57], v[56:57], v[170:171]
	v_cvt_pk_bf16_f32 v170, v54, v55
	v_cvt_pk_bf16_f32 v171, v56, v57
	global_store_dwordx2 v226, v[170:171], s[22:23] offset:3072
	v_fmac_f32_e32 v126, v54, v54
	v_fmac_f32_e32 v126, v55, v55
	v_fmac_f32_e32 v126, v56, v56
	v_fmac_f32_e32 v126, v57, v57
	s_waitcnt vmcnt(55)
	v_lshlrev_b32_e32 v44, 16, v172
	v_and_b32_e32 v45, 0xffff0000, v172
	v_lshlrev_b32_e32 v172, 16, v173
	v_and_b32_e32 v173, 0xffff0000, v173
	v_pk_add_f32 v[58:59], v[58:59], v[44:45]
	v_pk_add_f32 v[60:61], v[60:61], v[172:173]
	v_cvt_pk_bf16_f32 v172, v58, v59
	v_cvt_pk_bf16_f32 v173, v60, v61
	global_store_dwordx2 v226, v[172:173], s[22:23] offset:3584
	v_fmac_f32_e32 v126, v58, v58
	v_fmac_f32_e32 v126, v59, v59
	v_fmac_f32_e32 v126, v60, v60
	v_fmac_f32_e32 v126, v61, v61
	s_waitcnt vmcnt(54)
	v_lshlrev_b32_e32 v44, 16, v174
	v_and_b32_e32 v45, 0xffff0000, v174
	v_lshlrev_b32_e32 v174, 16, v175
	v_and_b32_e32 v175, 0xffff0000, v175
	v_pk_add_f32 v[20:21], v[20:21], v[44:45]
	v_pk_add_f32 v[22:23], v[22:23], v[174:175]
	v_cvt_pk_bf16_f32 v174, v20, v21
	v_cvt_pk_bf16_f32 v175, v22, v23
	global_store_dwordx2 v227, v[174:175], s[22:23] offset:0
	v_mul_f32_e32 v127, v20, v20
	v_fmac_f32_e32 v127, v21, v21
	v_fmac_f32_e32 v127, v22, v22
	v_fmac_f32_e32 v127, v23, v23
	s_waitcnt vmcnt(53)
	v_lshlrev_b32_e32 v44, 16, v176
	v_and_b32_e32 v45, 0xffff0000, v176
	v_lshlrev_b32_e32 v176, 16, v177
	v_and_b32_e32 v177, 0xffff0000, v177
	v_pk_add_f32 v[24:25], v[24:25], v[44:45]
	v_pk_add_f32 v[26:27], v[26:27], v[176:177]
	v_cvt_pk_bf16_f32 v176, v24, v25
	v_cvt_pk_bf16_f32 v177, v26, v27
	global_store_dwordx2 v227, v[176:177], s[22:23] offset:512
	v_fmac_f32_e32 v127, v24, v24
	v_fmac_f32_e32 v127, v25, v25
	v_fmac_f32_e32 v127, v26, v26
	v_fmac_f32_e32 v127, v27, v27
	s_waitcnt vmcnt(52)
	v_lshlrev_b32_e32 v44, 16, v178
	v_and_b32_e32 v45, 0xffff0000, v178
	v_lshlrev_b32_e32 v178, 16, v179
	v_and_b32_e32 v179, 0xffff0000, v179
	v_pk_add_f32 v[28:29], v[28:29], v[44:45]
	v_pk_add_f32 v[30:31], v[30:31], v[178:179]
	v_cvt_pk_bf16_f32 v178, v28, v29
	v_cvt_pk_bf16_f32 v179, v30, v31
	global_store_dwordx2 v227, v[178:179], s[22:23] offset:1024
	v_fmac_f32_e32 v127, v28, v28
	v_fmac_f32_e32 v127, v29, v29
	v_fmac_f32_e32 v127, v30, v30
	v_fmac_f32_e32 v127, v31, v31
	s_waitcnt vmcnt(51)
	v_lshlrev_b32_e32 v44, 16, v180
	v_and_b32_e32 v45, 0xffff0000, v180
	v_lshlrev_b32_e32 v180, 16, v181
	v_and_b32_e32 v181, 0xffff0000, v181
	v_pk_add_f32 v[32:33], v[32:33], v[44:45]
	v_pk_add_f32 v[34:35], v[34:35], v[180:181]
	v_cvt_pk_bf16_f32 v180, v32, v33
	v_cvt_pk_bf16_f32 v181, v34, v35
	global_store_dwordx2 v227, v[180:181], s[22:23] offset:1536
	v_fmac_f32_e32 v127, v32, v32
	v_fmac_f32_e32 v127, v33, v33
	v_fmac_f32_e32 v127, v34, v34
	v_fmac_f32_e32 v127, v35, v35
	s_waitcnt vmcnt(50)
	v_lshlrev_b32_e32 v44, 16, v182
	v_and_b32_e32 v45, 0xffff0000, v182
	v_lshlrev_b32_e32 v182, 16, v183
	v_and_b32_e32 v183, 0xffff0000, v183
	v_pk_add_f32 v[62:63], v[62:63], v[44:45]
	v_pk_add_f32 v[64:65], v[64:65], v[182:183]
	v_cvt_pk_bf16_f32 v182, v62, v63
	v_cvt_pk_bf16_f32 v183, v64, v65
	global_store_dwordx2 v227, v[182:183], s[22:23] offset:2048
	v_fmac_f32_e32 v127, v62, v62
	v_fmac_f32_e32 v127, v63, v63
	v_fmac_f32_e32 v127, v64, v64
	v_fmac_f32_e32 v127, v65, v65
	s_waitcnt vmcnt(49)
	v_lshlrev_b32_e32 v44, 16, v184
	v_and_b32_e32 v45, 0xffff0000, v184
	v_lshlrev_b32_e32 v184, 16, v185
	v_and_b32_e32 v185, 0xffff0000, v185
	v_pk_add_f32 v[66:67], v[66:67], v[44:45]
	v_pk_add_f32 v[68:69], v[68:69], v[184:185]
	v_cvt_pk_bf16_f32 v184, v66, v67
	v_cvt_pk_bf16_f32 v185, v68, v69
	global_store_dwordx2 v227, v[184:185], s[22:23] offset:2560
	v_fmac_f32_e32 v127, v66, v66
	v_fmac_f32_e32 v127, v67, v67
	v_fmac_f32_e32 v127, v68, v68
	v_fmac_f32_e32 v127, v69, v69
	s_waitcnt vmcnt(48)
	v_lshlrev_b32_e32 v44, 16, v186
	v_and_b32_e32 v45, 0xffff0000, v186
	v_lshlrev_b32_e32 v186, 16, v187
	v_and_b32_e32 v187, 0xffff0000, v187
	v_pk_add_f32 v[70:71], v[70:71], v[44:45]
	v_pk_add_f32 v[72:73], v[72:73], v[186:187]
	v_cvt_pk_bf16_f32 v186, v70, v71
	v_cvt_pk_bf16_f32 v187, v72, v73
	global_store_dwordx2 v227, v[186:187], s[22:23] offset:3072
	v_fmac_f32_e32 v127, v70, v70
	v_fmac_f32_e32 v127, v71, v71
	v_fmac_f32_e32 v127, v72, v72
	v_fmac_f32_e32 v127, v73, v73
	s_waitcnt vmcnt(47)
	v_lshlrev_b32_e32 v44, 16, v188
	v_and_b32_e32 v45, 0xffff0000, v188
	v_lshlrev_b32_e32 v188, 16, v189
	v_and_b32_e32 v189, 0xffff0000, v189
	v_pk_add_f32 v[74:75], v[74:75], v[44:45]
	v_pk_add_f32 v[76:77], v[76:77], v[188:189]
	v_cvt_pk_bf16_f32 v188, v74, v75
	v_cvt_pk_bf16_f32 v189, v76, v77
	global_store_dwordx2 v227, v[188:189], s[22:23] offset:3584
	v_fmac_f32_e32 v127, v74, v74
	v_fmac_f32_e32 v127, v75, v75
	v_fmac_f32_e32 v127, v76, v76
	v_fmac_f32_e32 v127, v77, v77
	s_waitcnt vmcnt(46)
	v_lshlrev_b32_e32 v44, 16, v190
	v_and_b32_e32 v45, 0xffff0000, v190
	v_lshlrev_b32_e32 v190, 16, v191
	v_and_b32_e32 v191, 0xffff0000, v191
	v_pk_add_f32 v[36:37], v[36:37], v[44:45]
	v_pk_add_f32 v[38:39], v[38:39], v[190:191]
	v_cvt_pk_bf16_f32 v190, v36, v37
	v_cvt_pk_bf16_f32 v191, v38, v39
	global_store_dwordx2 v228, v[190:191], s[22:23] offset:0
	v_mul_f32_e32 v158, v36, v36
	v_fmac_f32_e32 v158, v37, v37
	v_fmac_f32_e32 v158, v38, v38
	v_fmac_f32_e32 v158, v39, v39
	s_waitcnt vmcnt(45)
	v_lshlrev_b32_e32 v44, 16, v192
	v_and_b32_e32 v45, 0xffff0000, v192
	v_lshlrev_b32_e32 v192, 16, v193
	v_and_b32_e32 v193, 0xffff0000, v193
	v_pk_add_f32 v[40:41], v[40:41], v[44:45]
	v_pk_add_f32 v[42:43], v[42:43], v[192:193]
	v_cvt_pk_bf16_f32 v192, v40, v41
	v_cvt_pk_bf16_f32 v193, v42, v43
	global_store_dwordx2 v228, v[192:193], s[22:23] offset:512
	v_fmac_f32_e32 v158, v40, v40
	v_fmac_f32_e32 v158, v41, v41
	v_fmac_f32_e32 v158, v42, v42
	v_fmac_f32_e32 v158, v43, v43
	s_waitcnt vmcnt(44)
	v_lshlrev_b32_e32 v44, 16, v194
	v_and_b32_e32 v45, 0xffff0000, v194
	v_lshlrev_b32_e32 v194, 16, v195
	v_and_b32_e32 v195, 0xffff0000, v195
	v_pk_add_f32 v[110:111], v[110:111], v[44:45]
	v_pk_add_f32 v[112:113], v[112:113], v[194:195]
	v_cvt_pk_bf16_f32 v194, v110, v111
	v_cvt_pk_bf16_f32 v195, v112, v113
	global_store_dwordx2 v228, v[194:195], s[22:23] offset:1024
	v_fmac_f32_e32 v158, v110, v110
	v_fmac_f32_e32 v158, v111, v111
	v_fmac_f32_e32 v158, v112, v112
	v_fmac_f32_e32 v158, v113, v113
	s_waitcnt vmcnt(43)
	v_lshlrev_b32_e32 v44, 16, v196
	v_and_b32_e32 v45, 0xffff0000, v196
	v_lshlrev_b32_e32 v196, 16, v197
	v_and_b32_e32 v197, 0xffff0000, v197
	v_pk_add_f32 v[114:115], v[114:115], v[44:45]
	v_pk_add_f32 v[116:117], v[116:117], v[196:197]
	v_cvt_pk_bf16_f32 v196, v114, v115
	v_cvt_pk_bf16_f32 v197, v116, v117
	global_store_dwordx2 v228, v[196:197], s[22:23] offset:1536
	v_fmac_f32_e32 v158, v114, v114
	v_fmac_f32_e32 v158, v115, v115
	v_fmac_f32_e32 v158, v116, v116
	v_fmac_f32_e32 v158, v117, v117
	s_waitcnt vmcnt(42)
	v_lshlrev_b32_e32 v44, 16, v198
	v_and_b32_e32 v45, 0xffff0000, v198
	v_lshlrev_b32_e32 v198, 16, v199
	v_and_b32_e32 v199, 0xffff0000, v199
	v_pk_add_f32 v[78:79], v[78:79], v[44:45]
	v_pk_add_f32 v[80:81], v[80:81], v[198:199]
	v_cvt_pk_bf16_f32 v198, v78, v79
	v_cvt_pk_bf16_f32 v199, v80, v81
	global_store_dwordx2 v228, v[198:199], s[22:23] offset:2048
	v_fmac_f32_e32 v158, v78, v78
	v_fmac_f32_e32 v158, v79, v79
	v_fmac_f32_e32 v158, v80, v80
	v_fmac_f32_e32 v158, v81, v81
	s_waitcnt vmcnt(41)
	v_lshlrev_b32_e32 v44, 16, v200
	v_and_b32_e32 v45, 0xffff0000, v200
	v_lshlrev_b32_e32 v200, 16, v201
	v_and_b32_e32 v201, 0xffff0000, v201
	v_pk_add_f32 v[82:83], v[82:83], v[44:45]
	v_pk_add_f32 v[84:85], v[84:85], v[200:201]
	v_cvt_pk_bf16_f32 v200, v82, v83
	v_cvt_pk_bf16_f32 v201, v84, v85
	global_store_dwordx2 v228, v[200:201], s[22:23] offset:2560
	v_fmac_f32_e32 v158, v82, v82
	v_fmac_f32_e32 v158, v83, v83
	v_fmac_f32_e32 v158, v84, v84
	v_fmac_f32_e32 v158, v85, v85
	s_waitcnt vmcnt(40)
	v_lshlrev_b32_e32 v44, 16, v202
	v_and_b32_e32 v45, 0xffff0000, v202
	v_lshlrev_b32_e32 v202, 16, v203
	v_and_b32_e32 v203, 0xffff0000, v203
	v_pk_add_f32 v[86:87], v[86:87], v[44:45]
	v_pk_add_f32 v[88:89], v[88:89], v[202:203]
	v_cvt_pk_bf16_f32 v202, v86, v87
	v_cvt_pk_bf16_f32 v203, v88, v89
	global_store_dwordx2 v228, v[202:203], s[22:23] offset:3072
	v_fmac_f32_e32 v158, v86, v86
	v_fmac_f32_e32 v158, v87, v87
	v_fmac_f32_e32 v158, v88, v88
	v_fmac_f32_e32 v158, v89, v89
	s_waitcnt vmcnt(39)
	v_lshlrev_b32_e32 v44, 16, v204
	v_and_b32_e32 v45, 0xffff0000, v204
	v_lshlrev_b32_e32 v204, 16, v205
	v_and_b32_e32 v205, 0xffff0000, v205
	v_pk_add_f32 v[90:91], v[90:91], v[44:45]
	v_pk_add_f32 v[92:93], v[92:93], v[204:205]
	v_cvt_pk_bf16_f32 v204, v90, v91
	v_cvt_pk_bf16_f32 v205, v92, v93
	global_store_dwordx2 v228, v[204:205], s[22:23] offset:3584
	v_fmac_f32_e32 v158, v90, v90
	v_fmac_f32_e32 v158, v91, v91
	v_fmac_f32_e32 v158, v92, v92
	v_fmac_f32_e32 v158, v93, v93
	s_waitcnt vmcnt(38)
	v_lshlrev_b32_e32 v44, 16, v206
	v_and_b32_e32 v45, 0xffff0000, v206
	v_lshlrev_b32_e32 v206, 16, v207
	v_and_b32_e32 v207, 0xffff0000, v207
	v_pk_add_f32 v[118:119], v[118:119], v[44:45]
	v_pk_add_f32 v[120:121], v[120:121], v[206:207]
	v_cvt_pk_bf16_f32 v206, v118, v119
	v_cvt_pk_bf16_f32 v207, v120, v121
	global_store_dwordx2 v229, v[206:207], s[22:23] offset:0
	v_mul_f32_e32 v159, v118, v118
	v_fmac_f32_e32 v159, v119, v119
	v_fmac_f32_e32 v159, v120, v120
	v_fmac_f32_e32 v159, v121, v121
	s_waitcnt vmcnt(37)
	v_lshlrev_b32_e32 v44, 16, v208
	v_and_b32_e32 v45, 0xffff0000, v208
	v_lshlrev_b32_e32 v208, 16, v209
	v_and_b32_e32 v209, 0xffff0000, v209
	v_pk_add_f32 v[122:123], v[122:123], v[44:45]
	v_pk_add_f32 v[124:125], v[124:125], v[208:209]
	v_cvt_pk_bf16_f32 v208, v122, v123
	v_cvt_pk_bf16_f32 v209, v124, v125
	global_store_dwordx2 v229, v[208:209], s[22:23] offset:512
	v_fmac_f32_e32 v159, v122, v122
	v_fmac_f32_e32 v159, v123, v123
	v_fmac_f32_e32 v159, v124, v124
	v_fmac_f32_e32 v159, v125, v125
	s_waitcnt vmcnt(36)
	v_lshlrev_b32_e32 v44, 16, v210
	v_and_b32_e32 v45, 0xffff0000, v210
	v_lshlrev_b32_e32 v210, 16, v211
	v_and_b32_e32 v211, 0xffff0000, v211
	v_pk_add_f32 v[150:151], v[150:151], v[44:45]
	v_pk_add_f32 v[152:153], v[152:153], v[210:211]
	v_cvt_pk_bf16_f32 v210, v150, v151
	v_cvt_pk_bf16_f32 v211, v152, v153
	global_store_dwordx2 v229, v[210:211], s[22:23] offset:1024
	v_fmac_f32_e32 v159, v150, v150
	v_fmac_f32_e32 v159, v151, v151
	v_fmac_f32_e32 v159, v152, v152
	v_fmac_f32_e32 v159, v153, v153
	s_waitcnt vmcnt(35)
	v_lshlrev_b32_e32 v44, 16, v212
	v_and_b32_e32 v45, 0xffff0000, v212
	v_lshlrev_b32_e32 v212, 16, v213
	v_and_b32_e32 v213, 0xffff0000, v213
	v_pk_add_f32 v[154:155], v[154:155], v[44:45]
	v_pk_add_f32 v[156:157], v[156:157], v[212:213]
	v_cvt_pk_bf16_f32 v212, v154, v155
	v_cvt_pk_bf16_f32 v213, v156, v157
	global_store_dwordx2 v229, v[212:213], s[22:23] offset:1536
	v_fmac_f32_e32 v159, v154, v154
	v_fmac_f32_e32 v159, v155, v155
	v_fmac_f32_e32 v159, v156, v156
	v_fmac_f32_e32 v159, v157, v157
	s_waitcnt vmcnt(34)
	v_lshlrev_b32_e32 v44, 16, v214
	v_and_b32_e32 v45, 0xffff0000, v214
	v_lshlrev_b32_e32 v214, 16, v215
	v_and_b32_e32 v215, 0xffff0000, v215
	v_pk_add_f32 v[94:95], v[94:95], v[44:45]
	v_pk_add_f32 v[96:97], v[96:97], v[214:215]
	v_cvt_pk_bf16_f32 v214, v94, v95
	v_cvt_pk_bf16_f32 v215, v96, v97
	global_store_dwordx2 v229, v[214:215], s[22:23] offset:2048
	v_fmac_f32_e32 v159, v94, v94
	v_fmac_f32_e32 v159, v95, v95
	v_fmac_f32_e32 v159, v96, v96
	v_fmac_f32_e32 v159, v97, v97
	s_waitcnt vmcnt(33)
	v_lshlrev_b32_e32 v44, 16, v216
	v_and_b32_e32 v45, 0xffff0000, v216
	v_lshlrev_b32_e32 v216, 16, v217
	v_and_b32_e32 v217, 0xffff0000, v217
	v_pk_add_f32 v[98:99], v[98:99], v[44:45]
	v_pk_add_f32 v[100:101], v[100:101], v[216:217]
	v_cvt_pk_bf16_f32 v216, v98, v99
	v_cvt_pk_bf16_f32 v217, v100, v101
	global_store_dwordx2 v229, v[216:217], s[22:23] offset:2560
	v_fmac_f32_e32 v159, v98, v98
	v_fmac_f32_e32 v159, v99, v99
	v_fmac_f32_e32 v159, v100, v100
	v_fmac_f32_e32 v159, v101, v101
	s_waitcnt vmcnt(32)
	v_lshlrev_b32_e32 v44, 16, v218
	v_and_b32_e32 v45, 0xffff0000, v218
	v_lshlrev_b32_e32 v218, 16, v219
	v_and_b32_e32 v219, 0xffff0000, v219
	v_pk_add_f32 v[102:103], v[102:103], v[44:45]
	v_pk_add_f32 v[104:105], v[104:105], v[218:219]
	v_cvt_pk_bf16_f32 v218, v102, v103
	v_cvt_pk_bf16_f32 v219, v104, v105
	global_store_dwordx2 v229, v[218:219], s[22:23] offset:3072
	v_fmac_f32_e32 v159, v102, v102
	v_fmac_f32_e32 v159, v103, v103
	v_fmac_f32_e32 v159, v104, v104
	v_fmac_f32_e32 v159, v105, v105
	s_waitcnt vmcnt(31)
	v_lshlrev_b32_e32 v44, 16, v220
	v_and_b32_e32 v45, 0xffff0000, v220
	v_lshlrev_b32_e32 v220, 16, v221
	v_and_b32_e32 v221, 0xffff0000, v221
	v_pk_add_f32 v[106:107], v[106:107], v[44:45]
	v_pk_add_f32 v[108:109], v[108:109], v[220:221]
	v_cvt_pk_bf16_f32 v220, v106, v107
	v_cvt_pk_bf16_f32 v221, v108, v109
	global_store_dwordx2 v229, v[220:221], s[22:23] offset:3584
	v_fmac_f32_e32 v159, v106, v106
	v_fmac_f32_e32 v159, v107, v107
	v_fmac_f32_e32 v159, v108, v108
	v_fmac_f32_e32 v159, v109, v109
	s_bfe_i32 s10, s57, 0x150006
	s_mul_i32 s10, s10, 0xc000
	s_add_u32 s100, s16, s10
	s_addc_u32 s101, s17, 0
	s_add_u32 s98, s100, 0x6000
	s_addc_u32 s99, s101, 0
	s_add_u32 s100, s100, 0x8000
	s_addc_u32 s101, s101, 0
	v_lshlrev_b32_e32 v214, 2, v128
	v_add_u32_e32 v215, 0x1000, v214
	global_load_dwordx4 v[170:173], v214, s[28:29] offset:0
	global_load_dwordx4 v[178:181], v214, s[100:101] offset:0
	global_load_dwordx4 v[186:189], v214, s[98:99] offset:0
	v_xor_b32_e32 v160, 0x80, v128
	v_xor_b32_e32 v161, 64, v128
	v_xor_b32_e32 v162, 32, v128
	v_xor_b32_e32 v163, 16, v128
	v_xor_b32_e32 v164, 8, v128
	v_xor_b32_e32 v165, 4, v128
	ds_bpermute_b32 v166, v160, v126
	ds_bpermute_b32 v167, v160, v127
	ds_bpermute_b32 v168, v160, v158
	ds_bpermute_b32 v169, v160, v159
	s_waitcnt lgkmcnt(0)
	v_add_f32_e32 v126, v126, v166
	v_add_f32_e32 v127, v127, v167
	v_add_f32_e32 v158, v158, v168
	v_add_f32_e32 v159, v159, v169
	ds_bpermute_b32 v166, v161, v126
	ds_bpermute_b32 v167, v161, v127
	ds_bpermute_b32 v168, v161, v158
	ds_bpermute_b32 v169, v161, v159
	s_waitcnt lgkmcnt(0)
	v_add_f32_e32 v126, v126, v166
	v_add_f32_e32 v127, v127, v167
	v_add_f32_e32 v158, v158, v168
	v_add_f32_e32 v159, v159, v169
	ds_bpermute_b32 v166, v162, v126
	ds_bpermute_b32 v167, v162, v127
	ds_bpermute_b32 v168, v162, v158
	ds_bpermute_b32 v169, v162, v159
	s_waitcnt lgkmcnt(0)
	v_add_f32_e32 v126, v126, v166
	v_add_f32_e32 v127, v127, v167
	v_add_f32_e32 v158, v158, v168
	v_add_f32_e32 v159, v159, v169
	ds_bpermute_b32 v166, v163, v126
	ds_bpermute_b32 v167, v163, v127
	ds_bpermute_b32 v168, v163, v158
	ds_bpermute_b32 v169, v163, v159
	s_waitcnt lgkmcnt(0)
	v_add_f32_e32 v126, v126, v166
	v_add_f32_e32 v127, v127, v167
	v_add_f32_e32 v158, v158, v168
	v_add_f32_e32 v159, v159, v169
	ds_bpermute_b32 v166, v164, v126
	ds_bpermute_b32 v167, v164, v127
	ds_bpermute_b32 v168, v164, v158
	ds_bpermute_b32 v169, v164, v159
	s_waitcnt lgkmcnt(0)
	v_add_f32_e32 v126, v126, v166
	v_add_f32_e32 v127, v127, v167
	v_add_f32_e32 v158, v158, v168
	v_add_f32_e32 v159, v159, v169
	ds_bpermute_b32 v166, v165, v126
	ds_bpermute_b32 v167, v165, v127
	ds_bpermute_b32 v168, v165, v158
	ds_bpermute_b32 v169, v165, v159
	s_waitcnt lgkmcnt(0)
	v_add_f32_e32 v126, v126, v166
	v_add_f32_e32 v127, v127, v167
	v_add_f32_e32 v158, v158, v168
	v_add_f32_e32 v159, v159, v169
	v_mov_b32_e32 v166, 0x358637bd
	v_fmamk_f32 v126, v126, 0x3a000000, v166
	v_mul_f32_e32 v167, 0x4b800000, v126
	v_cmp_gt_f32_e32 vcc, 0x800000, v126
	s_nop 1
	v_cndmask_b32_e32 v126, v126, v167, vcc
	v_rsq_f32_e32 v126, v126
	s_nop 0
	v_mul_f32_e32 v167, 0x45800000, v126
	v_cndmask_b32_e32 v126, v126, v167, vcc
	v_fmamk_f32 v127, v127, 0x3a000000, v166
	v_mul_f32_e32 v168, 0x4b800000, v127
	v_cmp_gt_f32_e32 vcc, 0x800000, v127
	s_nop 1
	v_cndmask_b32_e32 v127, v127, v168, vcc
	v_rsq_f32_e32 v127, v127
	s_nop 0
	v_mul_f32_e32 v168, 0x45800000, v127
	v_cndmask_b32_e32 v127, v127, v168, vcc
	v_fmamk_f32 v158, v158, 0x3a000000, v166
	v_mul_f32_e32 v167, 0x4b800000, v158
	v_cmp_gt_f32_e32 vcc, 0x800000, v158
	s_nop 1
	v_cndmask_b32_e32 v158, v158, v167, vcc
	v_rsq_f32_e32 v158, v158
	s_nop 0
	v_mul_f32_e32 v167, 0x45800000, v158
	v_cndmask_b32_e32 v158, v158, v167, vcc
	v_fmamk_f32 v159, v159, 0x3a000000, v166
	v_mul_f32_e32 v168, 0x4b800000, v159
	v_cmp_gt_f32_e32 vcc, 0x800000, v159
	s_nop 1
	v_cndmask_b32_e32 v159, v159, v168, vcc
	v_rsq_f32_e32 v159, v159
	s_nop 0
	v_mul_f32_e32 v168, 0x45800000, v159
	v_cndmask_b32_e32 v159, v159, v168, vcc
	global_load_dwordx4 v[174:177], v214, s[28:29] offset:1024
	global_load_dwordx4 v[182:185], v214, s[100:101] offset:1024
	global_load_dwordx4 v[190:193], v214, s[98:99] offset:1024
	s_waitcnt vmcnt(3)
	v_add_f32_e32 v194, 1.0, v178
	v_add_f32_e32 v195, 1.0, v179
	v_add_f32_e32 v196, 1.0, v180
	v_add_f32_e32 v197, 1.0, v181
	v_mov_b32_e32 v213, v232
	v_mul_f32_e32 v4, v4, v126
	v_mul_f32_e32 v5, v5, v126
	v_mul_f32_e32 v6, v6, v126
	v_mul_f32_e32 v7, v7, v126
	v_mul_f32_e32 v4, v170, v4
	v_mul_f32_e32 v5, v171, v5
	v_mul_f32_e32 v6, v172, v6
	v_mul_f32_e32 v7, v173, v7
	v_fma_f32 v4, v4, v194, v186
	v_fma_f32 v5, v5, v195, v187
	v_fma_f32 v6, v6, v196, v188
	v_fma_f32 v7, v7, v197, v189
	v_cvt_pk_bf16_f32 v202, v4, v5
	v_cvt_pk_bf16_f32 v203, v6, v7
	v_mov_b32_e32 v210, 0
	v_cvt_pk_fp8_f32 v210, v4, v5
	v_cvt_pk_fp8_f32 v210, v6, v7 op_sel:[0,0,1]
	v_lshlrev_b32_e32 v198, 16, v202
	v_and_b32_e32 v199, 0xffff0000, v202
	v_lshlrev_b32_e32 v200, 16, v203
	v_and_b32_e32 v201, 0xffff0000, v203
	v_sub_f32_e32 v198, v4, v198
	v_sub_f32_e32 v199, v5, v199
	v_sub_f32_e32 v200, v6, v200
	v_sub_f32_e32 v201, v7, v201
	v_cvt_pk_bf16_f32 v208, v198, v199
	v_cvt_pk_bf16_f32 v209, v200, v201
	global_store_dword v230, v210, s[24:25] offset:0
	v_xor_b32_e32 v211, v213, v129
	v_lshl_add_u32 v211, v211, 4, v240
	v_add_u32_e32 v212, s56, v211
	ds_write_b64 v211, v[202:203]
	ds_write_b64 v212, v[208:209]
	v_mul_f32_e32 v20, v20, v127
	v_mul_f32_e32 v21, v21, v127
	v_mul_f32_e32 v22, v22, v127
	v_mul_f32_e32 v23, v23, v127
	v_mul_f32_e32 v20, v170, v20
	v_mul_f32_e32 v21, v171, v21
	v_mul_f32_e32 v22, v172, v22
	v_mul_f32_e32 v23, v173, v23
	v_fma_f32 v20, v20, v194, v186
	v_fma_f32 v21, v21, v195, v187
	v_fma_f32 v22, v22, v196, v188
	v_fma_f32 v23, v23, v197, v189
	v_cvt_pk_bf16_f32 v202, v20, v21
	v_cvt_pk_bf16_f32 v203, v22, v23
	v_mov_b32_e32 v210, 0
	v_cvt_pk_fp8_f32 v210, v20, v21
	v_cvt_pk_fp8_f32 v210, v22, v23 op_sel:[0,0,1]
	v_lshlrev_b32_e32 v198, 16, v202
	v_and_b32_e32 v199, 0xffff0000, v202
	v_lshlrev_b32_e32 v200, 16, v203
	v_and_b32_e32 v201, 0xffff0000, v203
	v_sub_f32_e32 v198, v20, v198
	v_sub_f32_e32 v199, v21, v199
	v_sub_f32_e32 v200, v22, v200
	v_sub_f32_e32 v201, v23, v201
	v_cvt_pk_bf16_f32 v208, v198, v199
	v_cvt_pk_bf16_f32 v209, v200, v201
	global_store_dword v231, v210, s[24:25] offset:0
	v_xor_b32_e32 v211, v213, v235
	v_lshl_add_u32 v211, v211, 4, v241
	v_add_u32_e32 v212, s56, v211
	ds_write_b64 v211, v[202:203]
	ds_write_b64 v212, v[208:209]
	v_mul_f32_e32 v36, v36, v158
	v_mul_f32_e32 v37, v37, v158
	v_mul_f32_e32 v38, v38, v158
	v_mul_f32_e32 v39, v39, v158
	v_mul_f32_e32 v36, v170, v36
	v_mul_f32_e32 v37, v171, v37
	v_mul_f32_e32 v38, v172, v38
	v_mul_f32_e32 v39, v173, v39
	v_fma_f32 v36, v36, v194, v186
	v_fma_f32 v37, v37, v195, v187
	v_fma_f32 v38, v38, v196, v188
	v_fma_f32 v39, v39, v197, v189
	v_cvt_pk_bf16_f32 v202, v36, v37
	v_cvt_pk_bf16_f32 v203, v38, v39
	v_mov_b32_e32 v210, 0
	v_cvt_pk_fp8_f32 v210, v36, v37
	v_cvt_pk_fp8_f32 v210, v38, v39 op_sel:[0,0,1]
	v_lshlrev_b32_e32 v198, 16, v202
	v_and_b32_e32 v199, 0xffff0000, v202
	v_lshlrev_b32_e32 v200, 16, v203
	v_and_b32_e32 v201, 0xffff0000, v203
	v_sub_f32_e32 v198, v36, v198
	v_sub_f32_e32 v199, v37, v199
	v_sub_f32_e32 v200, v38, v200
	v_sub_f32_e32 v201, v39, v201
	v_cvt_pk_bf16_f32 v208, v198, v199
	v_cvt_pk_bf16_f32 v209, v200, v201
	global_store_dword v0, v210, s[24:25] offset:0
	v_xor_b32_e32 v211, v213, v236
	v_lshl_add_u32 v211, v211, 4, v242
	v_add_u32_e32 v212, s56, v211
	ds_write_b64 v211, v[202:203]
	ds_write_b64 v212, v[208:209]
	v_mul_f32_e32 v118, v118, v159
	v_mul_f32_e32 v119, v119, v159
	v_mul_f32_e32 v120, v120, v159
	v_mul_f32_e32 v121, v121, v159
	v_mul_f32_e32 v118, v170, v118
	v_mul_f32_e32 v119, v171, v119
	v_mul_f32_e32 v120, v172, v120
	v_mul_f32_e32 v121, v173, v121
	v_fma_f32 v118, v118, v194, v186
	v_fma_f32 v119, v119, v195, v187
	v_fma_f32 v120, v120, v196, v188
	v_fma_f32 v121, v121, v197, v189
	v_cvt_pk_bf16_f32 v202, v118, v119
	v_cvt_pk_bf16_f32 v203, v120, v121
	v_mov_b32_e32 v210, 0
	v_cvt_pk_fp8_f32 v210, v118, v119
	v_cvt_pk_fp8_f32 v210, v120, v121 op_sel:[0,0,1]
	v_lshlrev_b32_e32 v198, 16, v202
	v_and_b32_e32 v199, 0xffff0000, v202
	v_lshlrev_b32_e32 v200, 16, v203
	v_and_b32_e32 v201, 0xffff0000, v203
	v_sub_f32_e32 v198, v118, v198
	v_sub_f32_e32 v199, v119, v199
	v_sub_f32_e32 v200, v120, v200
	v_sub_f32_e32 v201, v121, v201
	v_cvt_pk_bf16_f32 v208, v198, v199
	v_cvt_pk_bf16_f32 v209, v200, v201
	global_store_dword v3, v210, s[24:25] offset:0
	v_xor_b32_e32 v211, v213, v237
	v_lshl_add_u32 v211, v211, 4, v243
	v_add_u32_e32 v212, s56, v211
	ds_write_b64 v211, v[202:203]
	ds_write_b64 v212, v[208:209]
	global_load_dwordx4 v[170:173], v214, s[28:29] offset:2048
	global_load_dwordx4 v[178:181], v214, s[100:101] offset:2048
	global_load_dwordx4 v[186:189], v214, s[98:99] offset:2048
	s_waitcnt vmcnt(7)
	v_add_f32_e32 v194, 1.0, v182
	v_add_f32_e32 v195, 1.0, v183
	v_add_f32_e32 v196, 1.0, v184
	v_add_f32_e32 v197, 1.0, v185
	v_add_u32_e32 v213, 32, v232
	v_mul_f32_e32 v8, v8, v126
	v_mul_f32_e32 v9, v9, v126
	v_mul_f32_e32 v10, v10, v126
	v_mul_f32_e32 v11, v11, v126
	v_mul_f32_e32 v8, v174, v8
	v_mul_f32_e32 v9, v175, v9
	v_mul_f32_e32 v10, v176, v10
	v_mul_f32_e32 v11, v177, v11
	v_fma_f32 v8, v8, v194, v190
	v_fma_f32 v9, v9, v195, v191
	v_fma_f32 v10, v10, v196, v192
	v_fma_f32 v11, v11, v197, v193
	v_cvt_pk_bf16_f32 v202, v8, v9
	v_cvt_pk_bf16_f32 v203, v10, v11
	v_mov_b32_e32 v210, 0
	v_cvt_pk_fp8_f32 v210, v8, v9
	v_cvt_pk_fp8_f32 v210, v10, v11 op_sel:[0,0,1]
	v_lshlrev_b32_e32 v198, 16, v202
	v_and_b32_e32 v199, 0xffff0000, v202
	v_lshlrev_b32_e32 v200, 16, v203
	v_and_b32_e32 v201, 0xffff0000, v203
	v_sub_f32_e32 v198, v8, v198
	v_sub_f32_e32 v199, v9, v199
	v_sub_f32_e32 v200, v10, v200
	v_sub_f32_e32 v201, v11, v201
	v_cvt_pk_bf16_f32 v208, v198, v199
	v_cvt_pk_bf16_f32 v209, v200, v201
	global_store_dword v230, v210, s[24:25] offset:256
	v_xor_b32_e32 v211, v213, v129
	v_lshl_add_u32 v211, v211, 4, v240
	v_add_u32_e32 v212, s56, v211
	ds_write_b64 v211, v[202:203]
	ds_write_b64 v212, v[208:209]
	v_mul_f32_e32 v24, v24, v127
	v_mul_f32_e32 v25, v25, v127
	v_mul_f32_e32 v26, v26, v127
	v_mul_f32_e32 v27, v27, v127
	v_mul_f32_e32 v24, v174, v24
	v_mul_f32_e32 v25, v175, v25
	v_mul_f32_e32 v26, v176, v26
	v_mul_f32_e32 v27, v177, v27
	v_fma_f32 v24, v24, v194, v190
	v_fma_f32 v25, v25, v195, v191
	v_fma_f32 v26, v26, v196, v192
	v_fma_f32 v27, v27, v197, v193
	v_cvt_pk_bf16_f32 v202, v24, v25
	v_cvt_pk_bf16_f32 v203, v26, v27
	v_mov_b32_e32 v210, 0
	v_cvt_pk_fp8_f32 v210, v24, v25
	v_cvt_pk_fp8_f32 v210, v26, v27 op_sel:[0,0,1]
	v_lshlrev_b32_e32 v198, 16, v202
	v_and_b32_e32 v199, 0xffff0000, v202
	v_lshlrev_b32_e32 v200, 16, v203
	v_and_b32_e32 v201, 0xffff0000, v203
	v_sub_f32_e32 v198, v24, v198
	v_sub_f32_e32 v199, v25, v199
	v_sub_f32_e32 v200, v26, v200
	v_sub_f32_e32 v201, v27, v201
	v_cvt_pk_bf16_f32 v208, v198, v199
	v_cvt_pk_bf16_f32 v209, v200, v201
	global_store_dword v231, v210, s[24:25] offset:256
	v_xor_b32_e32 v211, v213, v235
	v_lshl_add_u32 v211, v211, 4, v241
	v_add_u32_e32 v212, s56, v211
	ds_write_b64 v211, v[202:203]
	ds_write_b64 v212, v[208:209]
	v_mul_f32_e32 v40, v40, v158
	v_mul_f32_e32 v41, v41, v158
	v_mul_f32_e32 v42, v42, v158
	v_mul_f32_e32 v43, v43, v158
	v_mul_f32_e32 v40, v174, v40
	v_mul_f32_e32 v41, v175, v41
	v_mul_f32_e32 v42, v176, v42
	v_mul_f32_e32 v43, v177, v43
	v_fma_f32 v40, v40, v194, v190
	v_fma_f32 v41, v41, v195, v191
	v_fma_f32 v42, v42, v196, v192
	v_fma_f32 v43, v43, v197, v193
	v_cvt_pk_bf16_f32 v202, v40, v41
	v_cvt_pk_bf16_f32 v203, v42, v43
	v_mov_b32_e32 v210, 0
	v_cvt_pk_fp8_f32 v210, v40, v41
	v_cvt_pk_fp8_f32 v210, v42, v43 op_sel:[0,0,1]
	v_lshlrev_b32_e32 v198, 16, v202
	v_and_b32_e32 v199, 0xffff0000, v202
	v_lshlrev_b32_e32 v200, 16, v203
	v_and_b32_e32 v201, 0xffff0000, v203
	v_sub_f32_e32 v198, v40, v198
	v_sub_f32_e32 v199, v41, v199
	v_sub_f32_e32 v200, v42, v200
	v_sub_f32_e32 v201, v43, v201
	v_cvt_pk_bf16_f32 v208, v198, v199
	v_cvt_pk_bf16_f32 v209, v200, v201
	global_store_dword v0, v210, s[24:25] offset:256
	v_xor_b32_e32 v211, v213, v236
	v_lshl_add_u32 v211, v211, 4, v242
	v_add_u32_e32 v212, s56, v211
	ds_write_b64 v211, v[202:203]
	ds_write_b64 v212, v[208:209]
	v_mul_f32_e32 v122, v122, v159
	v_mul_f32_e32 v123, v123, v159
	v_mul_f32_e32 v124, v124, v159
	v_mul_f32_e32 v125, v125, v159
	v_mul_f32_e32 v122, v174, v122
	v_mul_f32_e32 v123, v175, v123
	v_mul_f32_e32 v124, v176, v124
	v_mul_f32_e32 v125, v177, v125
	v_fma_f32 v122, v122, v194, v190
	v_fma_f32 v123, v123, v195, v191
	v_fma_f32 v124, v124, v196, v192
	v_fma_f32 v125, v125, v197, v193
	v_cvt_pk_bf16_f32 v202, v122, v123
	v_cvt_pk_bf16_f32 v203, v124, v125
	v_mov_b32_e32 v210, 0
	v_cvt_pk_fp8_f32 v210, v122, v123
	v_cvt_pk_fp8_f32 v210, v124, v125 op_sel:[0,0,1]
	v_lshlrev_b32_e32 v198, 16, v202
	v_and_b32_e32 v199, 0xffff0000, v202
	v_lshlrev_b32_e32 v200, 16, v203
	v_and_b32_e32 v201, 0xffff0000, v203
	v_sub_f32_e32 v198, v122, v198
	v_sub_f32_e32 v199, v123, v199
	v_sub_f32_e32 v200, v124, v200
	v_sub_f32_e32 v201, v125, v201
	v_cvt_pk_bf16_f32 v208, v198, v199
	v_cvt_pk_bf16_f32 v209, v200, v201
	global_store_dword v3, v210, s[24:25] offset:256
	v_xor_b32_e32 v211, v213, v237
	v_lshl_add_u32 v211, v211, 4, v243
	v_add_u32_e32 v212, s56, v211
	ds_write_b64 v211, v[202:203]
	ds_write_b64 v212, v[208:209]
	global_load_dwordx4 v[174:177], v214, s[28:29] offset:3072
	global_load_dwordx4 v[182:185], v214, s[100:101] offset:3072
	global_load_dwordx4 v[190:193], v214, s[98:99] offset:3072
	s_waitcnt vmcnt(7)
	v_add_f32_e32 v194, 1.0, v178
	v_add_f32_e32 v195, 1.0, v179
	v_add_f32_e32 v196, 1.0, v180
	v_add_f32_e32 v197, 1.0, v181
	v_add_u32_e32 v213, 64, v232
	v_mul_f32_e32 v12, v12, v126
	v_mul_f32_e32 v13, v13, v126
	v_mul_f32_e32 v14, v14, v126
	v_mul_f32_e32 v15, v15, v126
	v_mul_f32_e32 v12, v170, v12
	v_mul_f32_e32 v13, v171, v13
	v_mul_f32_e32 v14, v172, v14
	v_mul_f32_e32 v15, v173, v15
	v_fma_f32 v12, v12, v194, v186
	v_fma_f32 v13, v13, v195, v187
	v_fma_f32 v14, v14, v196, v188
	v_fma_f32 v15, v15, v197, v189
	v_cvt_pk_bf16_f32 v202, v12, v13
	v_cvt_pk_bf16_f32 v203, v14, v15
	v_mov_b32_e32 v210, 0
	v_cvt_pk_fp8_f32 v210, v12, v13
	v_cvt_pk_fp8_f32 v210, v14, v15 op_sel:[0,0,1]
	v_lshlrev_b32_e32 v198, 16, v202
	v_and_b32_e32 v199, 0xffff0000, v202
	v_lshlrev_b32_e32 v200, 16, v203
	v_and_b32_e32 v201, 0xffff0000, v203
	v_sub_f32_e32 v198, v12, v198
	v_sub_f32_e32 v199, v13, v199
	v_sub_f32_e32 v200, v14, v200
	v_sub_f32_e32 v201, v15, v201
	v_cvt_pk_bf16_f32 v208, v198, v199
	v_cvt_pk_bf16_f32 v209, v200, v201
	global_store_dword v230, v210, s[24:25] offset:512
	v_xor_b32_e32 v211, v213, v129
	v_lshl_add_u32 v211, v211, 4, v240
	v_add_u32_e32 v212, s56, v211
	ds_write_b64 v211, v[202:203]
	ds_write_b64 v212, v[208:209]
	v_mul_f32_e32 v28, v28, v127
	v_mul_f32_e32 v29, v29, v127
	v_mul_f32_e32 v30, v30, v127
	v_mul_f32_e32 v31, v31, v127
	v_mul_f32_e32 v28, v170, v28
	v_mul_f32_e32 v29, v171, v29
	v_mul_f32_e32 v30, v172, v30
	v_mul_f32_e32 v31, v173, v31
	v_fma_f32 v28, v28, v194, v186
	v_fma_f32 v29, v29, v195, v187
	v_fma_f32 v30, v30, v196, v188
	v_fma_f32 v31, v31, v197, v189
	v_cvt_pk_bf16_f32 v202, v28, v29
	v_cvt_pk_bf16_f32 v203, v30, v31
	v_mov_b32_e32 v210, 0
	v_cvt_pk_fp8_f32 v210, v28, v29
	v_cvt_pk_fp8_f32 v210, v30, v31 op_sel:[0,0,1]
	v_lshlrev_b32_e32 v198, 16, v202
	v_and_b32_e32 v199, 0xffff0000, v202
	v_lshlrev_b32_e32 v200, 16, v203
	v_and_b32_e32 v201, 0xffff0000, v203
	v_sub_f32_e32 v198, v28, v198
	v_sub_f32_e32 v199, v29, v199
	v_sub_f32_e32 v200, v30, v200
	v_sub_f32_e32 v201, v31, v201
	v_cvt_pk_bf16_f32 v208, v198, v199
	v_cvt_pk_bf16_f32 v209, v200, v201
	global_store_dword v231, v210, s[24:25] offset:512
	v_xor_b32_e32 v211, v213, v235
	v_lshl_add_u32 v211, v211, 4, v241
	v_add_u32_e32 v212, s56, v211
	ds_write_b64 v211, v[202:203]
	ds_write_b64 v212, v[208:209]
	v_mul_f32_e32 v110, v110, v158
	v_mul_f32_e32 v111, v111, v158
	v_mul_f32_e32 v112, v112, v158
	v_mul_f32_e32 v113, v113, v158
	v_mul_f32_e32 v110, v170, v110
	v_mul_f32_e32 v111, v171, v111
	v_mul_f32_e32 v112, v172, v112
	v_mul_f32_e32 v113, v173, v113
	v_fma_f32 v110, v110, v194, v186
	v_fma_f32 v111, v111, v195, v187
	v_fma_f32 v112, v112, v196, v188
	v_fma_f32 v113, v113, v197, v189
	v_cvt_pk_bf16_f32 v202, v110, v111
	v_cvt_pk_bf16_f32 v203, v112, v113
	v_mov_b32_e32 v210, 0
	v_cvt_pk_fp8_f32 v210, v110, v111
	v_cvt_pk_fp8_f32 v210, v112, v113 op_sel:[0,0,1]
	v_lshlrev_b32_e32 v198, 16, v202
	v_and_b32_e32 v199, 0xffff0000, v202
	v_lshlrev_b32_e32 v200, 16, v203
	v_and_b32_e32 v201, 0xffff0000, v203
	v_sub_f32_e32 v198, v110, v198
	v_sub_f32_e32 v199, v111, v199
	v_sub_f32_e32 v200, v112, v200
	v_sub_f32_e32 v201, v113, v201
	v_cvt_pk_bf16_f32 v208, v198, v199
	v_cvt_pk_bf16_f32 v209, v200, v201
	global_store_dword v0, v210, s[24:25] offset:512
	v_xor_b32_e32 v211, v213, v236
	v_lshl_add_u32 v211, v211, 4, v242
	v_add_u32_e32 v212, s56, v211
	ds_write_b64 v211, v[202:203]
	ds_write_b64 v212, v[208:209]
	v_mul_f32_e32 v150, v150, v159
	v_mul_f32_e32 v151, v151, v159
	v_mul_f32_e32 v152, v152, v159
	v_mul_f32_e32 v153, v153, v159
	v_mul_f32_e32 v150, v170, v150
	v_mul_f32_e32 v151, v171, v151
	v_mul_f32_e32 v152, v172, v152
	v_mul_f32_e32 v153, v173, v153
	v_fma_f32 v150, v150, v194, v186
	v_fma_f32 v151, v151, v195, v187
	v_fma_f32 v152, v152, v196, v188
	v_fma_f32 v153, v153, v197, v189
	v_cvt_pk_bf16_f32 v202, v150, v151
	v_cvt_pk_bf16_f32 v203, v152, v153
	v_mov_b32_e32 v210, 0
	v_cvt_pk_fp8_f32 v210, v150, v151
	v_cvt_pk_fp8_f32 v210, v152, v153 op_sel:[0,0,1]
	v_lshlrev_b32_e32 v198, 16, v202
	v_and_b32_e32 v199, 0xffff0000, v202
	v_lshlrev_b32_e32 v200, 16, v203
	v_and_b32_e32 v201, 0xffff0000, v203
	v_sub_f32_e32 v198, v150, v198
	v_sub_f32_e32 v199, v151, v199
	v_sub_f32_e32 v200, v152, v200
	v_sub_f32_e32 v201, v153, v201
	v_cvt_pk_bf16_f32 v208, v198, v199
	v_cvt_pk_bf16_f32 v209, v200, v201
	global_store_dword v3, v210, s[24:25] offset:512
	v_xor_b32_e32 v211, v213, v237
	v_lshl_add_u32 v211, v211, 4, v243
	v_add_u32_e32 v212, s56, v211
	ds_write_b64 v211, v[202:203]
	ds_write_b64 v212, v[208:209]
	global_load_dwordx4 v[170:173], v215, s[28:29] offset:0
	global_load_dwordx4 v[178:181], v215, s[100:101] offset:0
	global_load_dwordx4 v[186:189], v215, s[98:99] offset:0
	s_waitcnt vmcnt(7)
	v_add_f32_e32 v194, 1.0, v182
	v_add_f32_e32 v195, 1.0, v183
	v_add_f32_e32 v196, 1.0, v184
	v_add_f32_e32 v197, 1.0, v185
	v_add_u32_e32 v213, 96, v232
	v_mul_f32_e32 v16, v16, v126
	v_mul_f32_e32 v17, v17, v126
	v_mul_f32_e32 v18, v18, v126
	v_mul_f32_e32 v19, v19, v126
	v_mul_f32_e32 v16, v174, v16
	v_mul_f32_e32 v17, v175, v17
	v_mul_f32_e32 v18, v176, v18
	v_mul_f32_e32 v19, v177, v19
	v_fma_f32 v16, v16, v194, v190
	v_fma_f32 v17, v17, v195, v191
	v_fma_f32 v18, v18, v196, v192
	v_fma_f32 v19, v19, v197, v193
	v_cvt_pk_bf16_f32 v202, v16, v17
	v_cvt_pk_bf16_f32 v203, v18, v19
	v_mov_b32_e32 v210, 0
	v_cvt_pk_fp8_f32 v210, v16, v17
	v_cvt_pk_fp8_f32 v210, v18, v19 op_sel:[0,0,1]
	v_lshlrev_b32_e32 v198, 16, v202
	v_and_b32_e32 v199, 0xffff0000, v202
	v_lshlrev_b32_e32 v200, 16, v203
	v_and_b32_e32 v201, 0xffff0000, v203
	v_sub_f32_e32 v198, v16, v198
	v_sub_f32_e32 v199, v17, v199
	v_sub_f32_e32 v200, v18, v200
	v_sub_f32_e32 v201, v19, v201
	v_cvt_pk_bf16_f32 v208, v198, v199
	v_cvt_pk_bf16_f32 v209, v200, v201
	global_store_dword v230, v210, s[24:25] offset:768
	v_xor_b32_e32 v211, v213, v129
	v_lshl_add_u32 v211, v211, 4, v240
	v_add_u32_e32 v212, s56, v211
	ds_write_b64 v211, v[202:203]
	ds_write_b64 v212, v[208:209]
	v_mul_f32_e32 v32, v32, v127
	v_mul_f32_e32 v33, v33, v127
	v_mul_f32_e32 v34, v34, v127
	v_mul_f32_e32 v35, v35, v127
	v_mul_f32_e32 v32, v174, v32
	v_mul_f32_e32 v33, v175, v33
	v_mul_f32_e32 v34, v176, v34
	v_mul_f32_e32 v35, v177, v35
	v_fma_f32 v32, v32, v194, v190
	v_fma_f32 v33, v33, v195, v191
	v_fma_f32 v34, v34, v196, v192
	v_fma_f32 v35, v35, v197, v193
	v_cvt_pk_bf16_f32 v202, v32, v33
	v_cvt_pk_bf16_f32 v203, v34, v35
	v_mov_b32_e32 v210, 0
	v_cvt_pk_fp8_f32 v210, v32, v33
	v_cvt_pk_fp8_f32 v210, v34, v35 op_sel:[0,0,1]
	v_lshlrev_b32_e32 v198, 16, v202
	v_and_b32_e32 v199, 0xffff0000, v202
	v_lshlrev_b32_e32 v200, 16, v203
	v_and_b32_e32 v201, 0xffff0000, v203
	v_sub_f32_e32 v198, v32, v198
	v_sub_f32_e32 v199, v33, v199
	v_sub_f32_e32 v200, v34, v200
	v_sub_f32_e32 v201, v35, v201
	v_cvt_pk_bf16_f32 v208, v198, v199
	v_cvt_pk_bf16_f32 v209, v200, v201
	global_store_dword v231, v210, s[24:25] offset:768
	v_xor_b32_e32 v211, v213, v235
	v_lshl_add_u32 v211, v211, 4, v241
	v_add_u32_e32 v212, s56, v211
	ds_write_b64 v211, v[202:203]
	ds_write_b64 v212, v[208:209]
	v_mul_f32_e32 v114, v114, v158
	v_mul_f32_e32 v115, v115, v158
	v_mul_f32_e32 v116, v116, v158
	v_mul_f32_e32 v117, v117, v158
	v_mul_f32_e32 v114, v174, v114
	v_mul_f32_e32 v115, v175, v115
	v_mul_f32_e32 v116, v176, v116
	v_mul_f32_e32 v117, v177, v117
	v_fma_f32 v114, v114, v194, v190
	v_fma_f32 v115, v115, v195, v191
	v_fma_f32 v116, v116, v196, v192
	v_fma_f32 v117, v117, v197, v193
	v_cvt_pk_bf16_f32 v202, v114, v115
	v_cvt_pk_bf16_f32 v203, v116, v117
	v_mov_b32_e32 v210, 0
	v_cvt_pk_fp8_f32 v210, v114, v115
	v_cvt_pk_fp8_f32 v210, v116, v117 op_sel:[0,0,1]
	v_lshlrev_b32_e32 v198, 16, v202
	v_and_b32_e32 v199, 0xffff0000, v202
	v_lshlrev_b32_e32 v200, 16, v203
	v_and_b32_e32 v201, 0xffff0000, v203
	v_sub_f32_e32 v198, v114, v198
	v_sub_f32_e32 v199, v115, v199
	v_sub_f32_e32 v200, v116, v200
	v_sub_f32_e32 v201, v117, v201
	v_cvt_pk_bf16_f32 v208, v198, v199
	v_cvt_pk_bf16_f32 v209, v200, v201
	global_store_dword v0, v210, s[24:25] offset:768
	v_xor_b32_e32 v211, v213, v236
	v_lshl_add_u32 v211, v211, 4, v242
	v_add_u32_e32 v212, s56, v211
	ds_write_b64 v211, v[202:203]
	ds_write_b64 v212, v[208:209]
	v_mul_f32_e32 v154, v154, v159
	v_mul_f32_e32 v155, v155, v159
	v_mul_f32_e32 v156, v156, v159
	v_mul_f32_e32 v157, v157, v159
	v_mul_f32_e32 v154, v174, v154
	v_mul_f32_e32 v155, v175, v155
	v_mul_f32_e32 v156, v176, v156
	v_mul_f32_e32 v157, v177, v157
	v_fma_f32 v154, v154, v194, v190
	v_fma_f32 v155, v155, v195, v191
	v_fma_f32 v156, v156, v196, v192
	v_fma_f32 v157, v157, v197, v193
	v_cvt_pk_bf16_f32 v202, v154, v155
	v_cvt_pk_bf16_f32 v203, v156, v157
	v_mov_b32_e32 v210, 0
	v_cvt_pk_fp8_f32 v210, v154, v155
	v_cvt_pk_fp8_f32 v210, v156, v157 op_sel:[0,0,1]
	v_lshlrev_b32_e32 v198, 16, v202
	v_and_b32_e32 v199, 0xffff0000, v202
	v_lshlrev_b32_e32 v200, 16, v203
	v_and_b32_e32 v201, 0xffff0000, v203
	v_sub_f32_e32 v198, v154, v198
	v_sub_f32_e32 v199, v155, v199
	v_sub_f32_e32 v200, v156, v200
	v_sub_f32_e32 v201, v157, v201
	v_cvt_pk_bf16_f32 v208, v198, v199
	v_cvt_pk_bf16_f32 v209, v200, v201
	global_store_dword v3, v210, s[24:25] offset:768
	v_xor_b32_e32 v211, v213, v237
	v_lshl_add_u32 v211, v211, 4, v243
	v_add_u32_e32 v212, s56, v211
	ds_write_b64 v211, v[202:203]
	ds_write_b64 v212, v[208:209]
	global_load_dwordx4 v[174:177], v215, s[28:29] offset:1024
	global_load_dwordx4 v[182:185], v215, s[100:101] offset:1024
	global_load_dwordx4 v[190:193], v215, s[98:99] offset:1024
	s_waitcnt vmcnt(7)
	v_add_f32_e32 v194, 1.0, v178
	v_add_f32_e32 v195, 1.0, v179
	v_add_f32_e32 v196, 1.0, v180
	v_add_f32_e32 v197, 1.0, v181
	v_mul_f32_e32 v46, v46, v126
	v_mul_f32_e32 v47, v47, v126
	v_mul_f32_e32 v48, v48, v126
	v_mul_f32_e32 v49, v49, v126
	v_mul_f32_e32 v46, v170, v46
	v_mul_f32_e32 v47, v171, v47
	v_mul_f32_e32 v48, v172, v48
	v_mul_f32_e32 v49, v173, v49
	v_fma_f32 v46, v46, v194, v186
	v_fma_f32 v47, v47, v195, v187
	v_fma_f32 v48, v48, v196, v188
	v_fma_f32 v49, v49, v197, v189
	v_cvt_pk_bf16_f32 v202, v46, v47
	v_cvt_pk_bf16_f32 v203, v48, v49
	v_mov_b32_e32 v210, 0
	v_cvt_pk_fp8_f32 v210, v46, v47
	v_cvt_pk_fp8_f32 v210, v48, v49 op_sel:[0,0,1]
	v_lshlrev_b32_e32 v198, 16, v202
	v_and_b32_e32 v199, 0xffff0000, v202
	v_lshlrev_b32_e32 v200, 16, v203
	v_and_b32_e32 v201, 0xffff0000, v203
	v_sub_f32_e32 v198, v46, v198
	v_sub_f32_e32 v199, v47, v199
	v_sub_f32_e32 v200, v48, v200
	v_sub_f32_e32 v201, v49, v201
	v_cvt_pk_bf16_f32 v208, v198, v199
	v_cvt_pk_bf16_f32 v209, v200, v201
	global_store_dword v230, v210, s[24:25] offset:1024
	v_mov_b32_e32 v46, v202
	v_mov_b32_e32 v47, v203
	v_mov_b32_e32 v48, v208
	v_mov_b32_e32 v49, v209
	v_mul_f32_e32 v62, v62, v127
	v_mul_f32_e32 v63, v63, v127
	v_mul_f32_e32 v64, v64, v127
	v_mul_f32_e32 v65, v65, v127
	v_mul_f32_e32 v62, v170, v62
	v_mul_f32_e32 v63, v171, v63
	v_mul_f32_e32 v64, v172, v64
	v_mul_f32_e32 v65, v173, v65
	v_fma_f32 v62, v62, v194, v186
	v_fma_f32 v63, v63, v195, v187
	v_fma_f32 v64, v64, v196, v188
	v_fma_f32 v65, v65, v197, v189
	v_cvt_pk_bf16_f32 v202, v62, v63
	v_cvt_pk_bf16_f32 v203, v64, v65
	v_mov_b32_e32 v210, 0
	v_cvt_pk_fp8_f32 v210, v62, v63
	v_cvt_pk_fp8_f32 v210, v64, v65 op_sel:[0,0,1]
	v_lshlrev_b32_e32 v198, 16, v202
	v_and_b32_e32 v199, 0xffff0000, v202
	v_lshlrev_b32_e32 v200, 16, v203
	v_and_b32_e32 v201, 0xffff0000, v203
	v_sub_f32_e32 v198, v62, v198
	v_sub_f32_e32 v199, v63, v199
	v_sub_f32_e32 v200, v64, v200
	v_sub_f32_e32 v201, v65, v201
	v_cvt_pk_bf16_f32 v208, v198, v199
	v_cvt_pk_bf16_f32 v209, v200, v201
	global_store_dword v231, v210, s[24:25] offset:1024
	v_mov_b32_e32 v62, v202
	v_mov_b32_e32 v63, v203
	v_mov_b32_e32 v64, v208
	v_mov_b32_e32 v65, v209
	v_mul_f32_e32 v78, v78, v158
	v_mul_f32_e32 v79, v79, v158
	v_mul_f32_e32 v80, v80, v158
	v_mul_f32_e32 v81, v81, v158
	v_mul_f32_e32 v78, v170, v78
	v_mul_f32_e32 v79, v171, v79
	v_mul_f32_e32 v80, v172, v80
	v_mul_f32_e32 v81, v173, v81
	v_fma_f32 v78, v78, v194, v186
	v_fma_f32 v79, v79, v195, v187
	v_fma_f32 v80, v80, v196, v188
	v_fma_f32 v81, v81, v197, v189
	v_cvt_pk_bf16_f32 v202, v78, v79
	v_cvt_pk_bf16_f32 v203, v80, v81
	v_mov_b32_e32 v210, 0
	v_cvt_pk_fp8_f32 v210, v78, v79
	v_cvt_pk_fp8_f32 v210, v80, v81 op_sel:[0,0,1]
	v_lshlrev_b32_e32 v198, 16, v202
	v_and_b32_e32 v199, 0xffff0000, v202
	v_lshlrev_b32_e32 v200, 16, v203
	v_and_b32_e32 v201, 0xffff0000, v203
	v_sub_f32_e32 v198, v78, v198
	v_sub_f32_e32 v199, v79, v199
	v_sub_f32_e32 v200, v80, v200
	v_sub_f32_e32 v201, v81, v201
	v_cvt_pk_bf16_f32 v208, v198, v199
	v_cvt_pk_bf16_f32 v209, v200, v201
	global_store_dword v0, v210, s[24:25] offset:1024
	v_mov_b32_e32 v78, v202
	v_mov_b32_e32 v79, v203
	v_mov_b32_e32 v80, v208
	v_mov_b32_e32 v81, v209
	v_mul_f32_e32 v94, v94, v159
	v_mul_f32_e32 v95, v95, v159
	v_mul_f32_e32 v96, v96, v159
	v_mul_f32_e32 v97, v97, v159
	v_mul_f32_e32 v94, v170, v94
	v_mul_f32_e32 v95, v171, v95
	v_mul_f32_e32 v96, v172, v96
	v_mul_f32_e32 v97, v173, v97
	v_fma_f32 v94, v94, v194, v186
	v_fma_f32 v95, v95, v195, v187
	v_fma_f32 v96, v96, v196, v188
	v_fma_f32 v97, v97, v197, v189
	v_cvt_pk_bf16_f32 v202, v94, v95
	v_cvt_pk_bf16_f32 v203, v96, v97
	v_mov_b32_e32 v210, 0
	v_cvt_pk_fp8_f32 v210, v94, v95
	v_cvt_pk_fp8_f32 v210, v96, v97 op_sel:[0,0,1]
	v_lshlrev_b32_e32 v198, 16, v202
	v_and_b32_e32 v199, 0xffff0000, v202
	v_lshlrev_b32_e32 v200, 16, v203
	v_and_b32_e32 v201, 0xffff0000, v203
	v_sub_f32_e32 v198, v94, v198
	v_sub_f32_e32 v199, v95, v199
	v_sub_f32_e32 v200, v96, v200
	v_sub_f32_e32 v201, v97, v201
	v_cvt_pk_bf16_f32 v208, v198, v199
	v_cvt_pk_bf16_f32 v209, v200, v201
	global_store_dword v3, v210, s[24:25] offset:1024
	v_mov_b32_e32 v94, v202
	v_mov_b32_e32 v95, v203
	v_mov_b32_e32 v96, v208
	v_mov_b32_e32 v97, v209
	global_load_dwordx4 v[170:173], v215, s[28:29] offset:2048
	global_load_dwordx4 v[178:181], v215, s[100:101] offset:2048
	global_load_dwordx4 v[186:189], v215, s[98:99] offset:2048
	s_waitcnt vmcnt(7)
	v_add_f32_e32 v194, 1.0, v182
	v_add_f32_e32 v195, 1.0, v183
	v_add_f32_e32 v196, 1.0, v184
	v_add_f32_e32 v197, 1.0, v185
	v_mul_f32_e32 v50, v50, v126
	v_mul_f32_e32 v51, v51, v126
	v_mul_f32_e32 v52, v52, v126
	v_mul_f32_e32 v53, v53, v126
	v_mul_f32_e32 v50, v174, v50
	v_mul_f32_e32 v51, v175, v51
	v_mul_f32_e32 v52, v176, v52
	v_mul_f32_e32 v53, v177, v53
	v_fma_f32 v50, v50, v194, v190
	v_fma_f32 v51, v51, v195, v191
	v_fma_f32 v52, v52, v196, v192
	v_fma_f32 v53, v53, v197, v193
	v_cvt_pk_bf16_f32 v202, v50, v51
	v_cvt_pk_bf16_f32 v203, v52, v53
	v_mov_b32_e32 v210, 0
	v_cvt_pk_fp8_f32 v210, v50, v51
	v_cvt_pk_fp8_f32 v210, v52, v53 op_sel:[0,0,1]
	v_lshlrev_b32_e32 v198, 16, v202
	v_and_b32_e32 v199, 0xffff0000, v202
	v_lshlrev_b32_e32 v200, 16, v203
	v_and_b32_e32 v201, 0xffff0000, v203
	v_sub_f32_e32 v198, v50, v198
	v_sub_f32_e32 v199, v51, v199
	v_sub_f32_e32 v200, v52, v200
	v_sub_f32_e32 v201, v53, v201
	v_cvt_pk_bf16_f32 v208, v198, v199
	v_cvt_pk_bf16_f32 v209, v200, v201
	global_store_dword v230, v210, s[24:25] offset:1280
	v_mov_b32_e32 v50, v202
	v_mov_b32_e32 v51, v203
	v_mov_b32_e32 v52, v208
	v_mov_b32_e32 v53, v209
	v_mul_f32_e32 v66, v66, v127
	v_mul_f32_e32 v67, v67, v127
	v_mul_f32_e32 v68, v68, v127
	v_mul_f32_e32 v69, v69, v127
	v_mul_f32_e32 v66, v174, v66
	v_mul_f32_e32 v67, v175, v67
	v_mul_f32_e32 v68, v176, v68
	v_mul_f32_e32 v69, v177, v69
	v_fma_f32 v66, v66, v194, v190
	v_fma_f32 v67, v67, v195, v191
	v_fma_f32 v68, v68, v196, v192
	v_fma_f32 v69, v69, v197, v193
	v_cvt_pk_bf16_f32 v202, v66, v67
	v_cvt_pk_bf16_f32 v203, v68, v69
	v_mov_b32_e32 v210, 0
	v_cvt_pk_fp8_f32 v210, v66, v67
	v_cvt_pk_fp8_f32 v210, v68, v69 op_sel:[0,0,1]
	v_lshlrev_b32_e32 v198, 16, v202
	v_and_b32_e32 v199, 0xffff0000, v202
	v_lshlrev_b32_e32 v200, 16, v203
	v_and_b32_e32 v201, 0xffff0000, v203
	v_sub_f32_e32 v198, v66, v198
	v_sub_f32_e32 v199, v67, v199
	v_sub_f32_e32 v200, v68, v200
	v_sub_f32_e32 v201, v69, v201
	v_cvt_pk_bf16_f32 v208, v198, v199
	v_cvt_pk_bf16_f32 v209, v200, v201
	global_store_dword v231, v210, s[24:25] offset:1280
	v_mov_b32_e32 v66, v202
	v_mov_b32_e32 v67, v203
	v_mov_b32_e32 v68, v208
	v_mov_b32_e32 v69, v209
	v_mul_f32_e32 v82, v82, v158
	v_mul_f32_e32 v83, v83, v158
	v_mul_f32_e32 v84, v84, v158
	v_mul_f32_e32 v85, v85, v158
	v_mul_f32_e32 v82, v174, v82
	v_mul_f32_e32 v83, v175, v83
	v_mul_f32_e32 v84, v176, v84
	v_mul_f32_e32 v85, v177, v85
	v_fma_f32 v82, v82, v194, v190
	v_fma_f32 v83, v83, v195, v191
	v_fma_f32 v84, v84, v196, v192
	v_fma_f32 v85, v85, v197, v193
	v_cvt_pk_bf16_f32 v202, v82, v83
	v_cvt_pk_bf16_f32 v203, v84, v85
	v_mov_b32_e32 v210, 0
	v_cvt_pk_fp8_f32 v210, v82, v83
	v_cvt_pk_fp8_f32 v210, v84, v85 op_sel:[0,0,1]
	v_lshlrev_b32_e32 v198, 16, v202
	v_and_b32_e32 v199, 0xffff0000, v202
	v_lshlrev_b32_e32 v200, 16, v203
	v_and_b32_e32 v201, 0xffff0000, v203
	v_sub_f32_e32 v198, v82, v198
	v_sub_f32_e32 v199, v83, v199
	v_sub_f32_e32 v200, v84, v200
	v_sub_f32_e32 v201, v85, v201
	v_cvt_pk_bf16_f32 v208, v198, v199
	v_cvt_pk_bf16_f32 v209, v200, v201
	global_store_dword v0, v210, s[24:25] offset:1280
	v_mov_b32_e32 v82, v202
	v_mov_b32_e32 v83, v203
	v_mov_b32_e32 v84, v208
	v_mov_b32_e32 v85, v209
	v_mul_f32_e32 v98, v98, v159
	v_mul_f32_e32 v99, v99, v159
	v_mul_f32_e32 v100, v100, v159
	v_mul_f32_e32 v101, v101, v159
	v_mul_f32_e32 v98, v174, v98
	v_mul_f32_e32 v99, v175, v99
	v_mul_f32_e32 v100, v176, v100
	v_mul_f32_e32 v101, v177, v101
	v_fma_f32 v98, v98, v194, v190
	v_fma_f32 v99, v99, v195, v191
	v_fma_f32 v100, v100, v196, v192
	v_fma_f32 v101, v101, v197, v193
	v_cvt_pk_bf16_f32 v202, v98, v99
	v_cvt_pk_bf16_f32 v203, v100, v101
	v_mov_b32_e32 v210, 0
	v_cvt_pk_fp8_f32 v210, v98, v99
	v_cvt_pk_fp8_f32 v210, v100, v101 op_sel:[0,0,1]
	v_lshlrev_b32_e32 v198, 16, v202
	v_and_b32_e32 v199, 0xffff0000, v202
	v_lshlrev_b32_e32 v200, 16, v203
	v_and_b32_e32 v201, 0xffff0000, v203
	v_sub_f32_e32 v198, v98, v198
	v_sub_f32_e32 v199, v99, v199
	v_sub_f32_e32 v200, v100, v200
	v_sub_f32_e32 v201, v101, v201
	v_cvt_pk_bf16_f32 v208, v198, v199
	v_cvt_pk_bf16_f32 v209, v200, v201
	global_store_dword v3, v210, s[24:25] offset:1280
	v_mov_b32_e32 v98, v202
	v_mov_b32_e32 v99, v203
	v_mov_b32_e32 v100, v208
	v_mov_b32_e32 v101, v209
	global_load_dwordx4 v[174:177], v215, s[28:29] offset:3072
	global_load_dwordx4 v[182:185], v215, s[100:101] offset:3072
	global_load_dwordx4 v[190:193], v215, s[98:99] offset:3072
	s_waitcnt vmcnt(7)
	v_add_f32_e32 v194, 1.0, v178
	v_add_f32_e32 v195, 1.0, v179
	v_add_f32_e32 v196, 1.0, v180
	v_add_f32_e32 v197, 1.0, v181
	v_mul_f32_e32 v54, v54, v126
	v_mul_f32_e32 v55, v55, v126
	v_mul_f32_e32 v56, v56, v126
	v_mul_f32_e32 v57, v57, v126
	v_mul_f32_e32 v54, v170, v54
	v_mul_f32_e32 v55, v171, v55
	v_mul_f32_e32 v56, v172, v56
	v_mul_f32_e32 v57, v173, v57
	v_fma_f32 v54, v54, v194, v186
	v_fma_f32 v55, v55, v195, v187
	v_fma_f32 v56, v56, v196, v188
	v_fma_f32 v57, v57, v197, v189
	v_cvt_pk_bf16_f32 v202, v54, v55
	v_cvt_pk_bf16_f32 v203, v56, v57
	v_mov_b32_e32 v210, 0
	v_cvt_pk_fp8_f32 v210, v54, v55
	v_cvt_pk_fp8_f32 v210, v56, v57 op_sel:[0,0,1]
	v_lshlrev_b32_e32 v198, 16, v202
	v_and_b32_e32 v199, 0xffff0000, v202
	v_lshlrev_b32_e32 v200, 16, v203
	v_and_b32_e32 v201, 0xffff0000, v203
	v_sub_f32_e32 v198, v54, v198
	v_sub_f32_e32 v199, v55, v199
	v_sub_f32_e32 v200, v56, v200
	v_sub_f32_e32 v201, v57, v201
	v_cvt_pk_bf16_f32 v208, v198, v199
	v_cvt_pk_bf16_f32 v209, v200, v201
	global_store_dword v230, v210, s[24:25] offset:1536
	v_mov_b32_e32 v54, v202
	v_mov_b32_e32 v55, v203
	v_mov_b32_e32 v56, v208
	v_mov_b32_e32 v57, v209
	v_mul_f32_e32 v70, v70, v127
	v_mul_f32_e32 v71, v71, v127
	v_mul_f32_e32 v72, v72, v127
	v_mul_f32_e32 v73, v73, v127
	v_mul_f32_e32 v70, v170, v70
	v_mul_f32_e32 v71, v171, v71
	v_mul_f32_e32 v72, v172, v72
	v_mul_f32_e32 v73, v173, v73
	v_fma_f32 v70, v70, v194, v186
	v_fma_f32 v71, v71, v195, v187
	v_fma_f32 v72, v72, v196, v188
	v_fma_f32 v73, v73, v197, v189
	v_cvt_pk_bf16_f32 v202, v70, v71
	v_cvt_pk_bf16_f32 v203, v72, v73
	v_mov_b32_e32 v210, 0
	v_cvt_pk_fp8_f32 v210, v70, v71
	v_cvt_pk_fp8_f32 v210, v72, v73 op_sel:[0,0,1]
	v_lshlrev_b32_e32 v198, 16, v202
	v_and_b32_e32 v199, 0xffff0000, v202
	v_lshlrev_b32_e32 v200, 16, v203
	v_and_b32_e32 v201, 0xffff0000, v203
	v_sub_f32_e32 v198, v70, v198
	v_sub_f32_e32 v199, v71, v199
	v_sub_f32_e32 v200, v72, v200
	v_sub_f32_e32 v201, v73, v201
	v_cvt_pk_bf16_f32 v208, v198, v199
	v_cvt_pk_bf16_f32 v209, v200, v201
	global_store_dword v231, v210, s[24:25] offset:1536
	v_mov_b32_e32 v70, v202
	v_mov_b32_e32 v71, v203
	v_mov_b32_e32 v72, v208
	v_mov_b32_e32 v73, v209
	v_mul_f32_e32 v86, v86, v158
	v_mul_f32_e32 v87, v87, v158
	v_mul_f32_e32 v88, v88, v158
	v_mul_f32_e32 v89, v89, v158
	v_mul_f32_e32 v86, v170, v86
	v_mul_f32_e32 v87, v171, v87
	v_mul_f32_e32 v88, v172, v88
	v_mul_f32_e32 v89, v173, v89
	v_fma_f32 v86, v86, v194, v186
	v_fma_f32 v87, v87, v195, v187
	v_fma_f32 v88, v88, v196, v188
	v_fma_f32 v89, v89, v197, v189
	v_cvt_pk_bf16_f32 v202, v86, v87
	v_cvt_pk_bf16_f32 v203, v88, v89
	v_mov_b32_e32 v210, 0
	v_cvt_pk_fp8_f32 v210, v86, v87
	v_cvt_pk_fp8_f32 v210, v88, v89 op_sel:[0,0,1]
	v_lshlrev_b32_e32 v198, 16, v202
	v_and_b32_e32 v199, 0xffff0000, v202
	v_lshlrev_b32_e32 v200, 16, v203
	v_and_b32_e32 v201, 0xffff0000, v203
	v_sub_f32_e32 v198, v86, v198
	v_sub_f32_e32 v199, v87, v199
	v_sub_f32_e32 v200, v88, v200
	v_sub_f32_e32 v201, v89, v201
	v_cvt_pk_bf16_f32 v208, v198, v199
	v_cvt_pk_bf16_f32 v209, v200, v201
	global_store_dword v0, v210, s[24:25] offset:1536
	v_mov_b32_e32 v86, v202
	v_mov_b32_e32 v87, v203
	v_mov_b32_e32 v88, v208
	v_mov_b32_e32 v89, v209
	v_mul_f32_e32 v102, v102, v159
	v_mul_f32_e32 v103, v103, v159
	v_mul_f32_e32 v104, v104, v159
	v_mul_f32_e32 v105, v105, v159
	v_mul_f32_e32 v102, v170, v102
	v_mul_f32_e32 v103, v171, v103
	v_mul_f32_e32 v104, v172, v104
	v_mul_f32_e32 v105, v173, v105
	v_fma_f32 v102, v102, v194, v186
	v_fma_f32 v103, v103, v195, v187
	v_fma_f32 v104, v104, v196, v188
	v_fma_f32 v105, v105, v197, v189
	v_cvt_pk_bf16_f32 v202, v102, v103
	v_cvt_pk_bf16_f32 v203, v104, v105
	v_mov_b32_e32 v210, 0
	v_cvt_pk_fp8_f32 v210, v102, v103
	v_cvt_pk_fp8_f32 v210, v104, v105 op_sel:[0,0,1]
	v_lshlrev_b32_e32 v198, 16, v202
	v_and_b32_e32 v199, 0xffff0000, v202
	v_lshlrev_b32_e32 v200, 16, v203
	v_and_b32_e32 v201, 0xffff0000, v203
	v_sub_f32_e32 v198, v102, v198
	v_sub_f32_e32 v199, v103, v199
	v_sub_f32_e32 v200, v104, v200
	v_sub_f32_e32 v201, v105, v201
	v_cvt_pk_bf16_f32 v208, v198, v199
	v_cvt_pk_bf16_f32 v209, v200, v201
	global_store_dword v3, v210, s[24:25] offset:1536
	v_mov_b32_e32 v102, v202
	v_mov_b32_e32 v103, v203
	v_mov_b32_e32 v104, v208
	v_mov_b32_e32 v105, v209
	s_waitcnt vmcnt(4)
	v_add_f32_e32 v194, 1.0, v182
	v_add_f32_e32 v195, 1.0, v183
	v_add_f32_e32 v196, 1.0, v184
	v_add_f32_e32 v197, 1.0, v185
	v_mul_f32_e32 v58, v58, v126
	v_mul_f32_e32 v59, v59, v126
	v_mul_f32_e32 v60, v60, v126
	v_mul_f32_e32 v61, v61, v126
	v_mul_f32_e32 v58, v174, v58
	v_mul_f32_e32 v59, v175, v59
	v_mul_f32_e32 v60, v176, v60
	v_mul_f32_e32 v61, v177, v61
	v_fma_f32 v58, v58, v194, v190
	v_fma_f32 v59, v59, v195, v191
	v_fma_f32 v60, v60, v196, v192
	v_fma_f32 v61, v61, v197, v193
	v_cvt_pk_bf16_f32 v202, v58, v59
	v_cvt_pk_bf16_f32 v203, v60, v61
	v_mov_b32_e32 v210, 0
	v_cvt_pk_fp8_f32 v210, v58, v59
	v_cvt_pk_fp8_f32 v210, v60, v61 op_sel:[0,0,1]
	v_lshlrev_b32_e32 v198, 16, v202
	v_and_b32_e32 v199, 0xffff0000, v202
	v_lshlrev_b32_e32 v200, 16, v203
	v_and_b32_e32 v201, 0xffff0000, v203
	v_sub_f32_e32 v198, v58, v198
	v_sub_f32_e32 v199, v59, v199
	v_sub_f32_e32 v200, v60, v200
	v_sub_f32_e32 v201, v61, v201
	v_cvt_pk_bf16_f32 v208, v198, v199
	v_cvt_pk_bf16_f32 v209, v200, v201
	global_store_dword v230, v210, s[24:25] offset:1792
	v_mov_b32_e32 v58, v202
	v_mov_b32_e32 v59, v203
	v_mov_b32_e32 v60, v208
	v_mov_b32_e32 v61, v209
	v_mul_f32_e32 v74, v74, v127
	v_mul_f32_e32 v75, v75, v127
	v_mul_f32_e32 v76, v76, v127
	v_mul_f32_e32 v77, v77, v127
	v_mul_f32_e32 v74, v174, v74
	v_mul_f32_e32 v75, v175, v75
	v_mul_f32_e32 v76, v176, v76
	v_mul_f32_e32 v77, v177, v77
	v_fma_f32 v74, v74, v194, v190
	v_fma_f32 v75, v75, v195, v191
	v_fma_f32 v76, v76, v196, v192
	v_fma_f32 v77, v77, v197, v193
	v_cvt_pk_bf16_f32 v202, v74, v75
	v_cvt_pk_bf16_f32 v203, v76, v77
	v_mov_b32_e32 v210, 0
	v_cvt_pk_fp8_f32 v210, v74, v75
	v_cvt_pk_fp8_f32 v210, v76, v77 op_sel:[0,0,1]
	v_lshlrev_b32_e32 v198, 16, v202
	v_and_b32_e32 v199, 0xffff0000, v202
	v_lshlrev_b32_e32 v200, 16, v203
	v_and_b32_e32 v201, 0xffff0000, v203
	v_sub_f32_e32 v198, v74, v198
	v_sub_f32_e32 v199, v75, v199
	v_sub_f32_e32 v200, v76, v200
	v_sub_f32_e32 v201, v77, v201
	v_cvt_pk_bf16_f32 v208, v198, v199
	v_cvt_pk_bf16_f32 v209, v200, v201
	global_store_dword v231, v210, s[24:25] offset:1792
	v_mov_b32_e32 v74, v202
	v_mov_b32_e32 v75, v203
	v_mov_b32_e32 v76, v208
	v_mov_b32_e32 v77, v209
	v_mul_f32_e32 v90, v90, v158
	v_mul_f32_e32 v91, v91, v158
	v_mul_f32_e32 v92, v92, v158
	v_mul_f32_e32 v93, v93, v158
	v_mul_f32_e32 v90, v174, v90
	v_mul_f32_e32 v91, v175, v91
	v_mul_f32_e32 v92, v176, v92
	v_mul_f32_e32 v93, v177, v93
	v_fma_f32 v90, v90, v194, v190
	v_fma_f32 v91, v91, v195, v191
	v_fma_f32 v92, v92, v196, v192
	v_fma_f32 v93, v93, v197, v193
	v_cvt_pk_bf16_f32 v202, v90, v91
	v_cvt_pk_bf16_f32 v203, v92, v93
	v_mov_b32_e32 v210, 0
	v_cvt_pk_fp8_f32 v210, v90, v91
	v_cvt_pk_fp8_f32 v210, v92, v93 op_sel:[0,0,1]
	v_lshlrev_b32_e32 v198, 16, v202
	v_and_b32_e32 v199, 0xffff0000, v202
	v_lshlrev_b32_e32 v200, 16, v203
	v_and_b32_e32 v201, 0xffff0000, v203
	v_sub_f32_e32 v198, v90, v198
	v_sub_f32_e32 v199, v91, v199
	v_sub_f32_e32 v200, v92, v200
	v_sub_f32_e32 v201, v93, v201
	v_cvt_pk_bf16_f32 v208, v198, v199
	v_cvt_pk_bf16_f32 v209, v200, v201
	global_store_dword v0, v210, s[24:25] offset:1792
	v_mov_b32_e32 v90, v202
	v_mov_b32_e32 v91, v203
	v_mov_b32_e32 v92, v208
	v_mov_b32_e32 v93, v209
	v_mul_f32_e32 v106, v106, v159
	v_mul_f32_e32 v107, v107, v159
	v_mul_f32_e32 v108, v108, v159
	v_mul_f32_e32 v109, v109, v159
	v_mul_f32_e32 v106, v174, v106
	v_mul_f32_e32 v107, v175, v107
	v_mul_f32_e32 v108, v176, v108
	v_mul_f32_e32 v109, v177, v109
	v_fma_f32 v106, v106, v194, v190
	v_fma_f32 v107, v107, v195, v191
	v_fma_f32 v108, v108, v196, v192
	v_fma_f32 v109, v109, v197, v193
	v_cvt_pk_bf16_f32 v202, v106, v107
	v_cvt_pk_bf16_f32 v203, v108, v109
	v_mov_b32_e32 v210, 0
	v_cvt_pk_fp8_f32 v210, v106, v107
	v_cvt_pk_fp8_f32 v210, v108, v109 op_sel:[0,0,1]
	v_lshlrev_b32_e32 v198, 16, v202
	v_and_b32_e32 v199, 0xffff0000, v202
	v_lshlrev_b32_e32 v200, 16, v203
	v_and_b32_e32 v201, 0xffff0000, v203
	v_sub_f32_e32 v198, v106, v198
	v_sub_f32_e32 v199, v107, v199
	v_sub_f32_e32 v200, v108, v200
	v_sub_f32_e32 v201, v109, v201
	v_cvt_pk_bf16_f32 v208, v198, v199
	v_cvt_pk_bf16_f32 v209, v200, v201
	global_store_dword v3, v210, s[24:25] offset:1792
	v_mov_b32_e32 v106, v202
	v_mov_b32_e32 v107, v203
	v_mov_b32_e32 v108, v208
	v_mov_b32_e32 v109, v209
	v_mov_b32_e32 v4, v2
	v_mov_b32_e32 v5, v2
	v_mov_b32_e32 v3, v2
	v_mov_b64_e32 v[8:9], v[4:5]
	v_mov_b64_e32 v[12:13], v[4:5]
	v_mov_b64_e32 v[16:17], v[4:5]
	v_mov_b64_e32 v[20:21], v[4:5]
	v_mov_b64_e32 v[24:25], v[4:5]
	v_mov_b64_e32 v[28:29], v[4:5]
	v_mov_b64_e32 v[6:7], v[2:3]
	v_mov_b64_e32 v[10:11], v[2:3]
	v_mov_b64_e32 v[14:15], v[2:3]
	v_mov_b64_e32 v[18:19], v[2:3]
	v_mov_b64_e32 v[22:23], v[2:3]
	v_mov_b64_e32 v[26:27], v[2:3]
	v_subrev_u32_e32 v222, s76, v136
	s_add_u32 s98, s76, 0x38178000
	s_addc_u32 s99, s77, 0
	s_add_u32 s100, s76, 0x381c8000
	s_addc_u32 s101, s77, 0
	v_add_u32_e32 v223, 0x10000, v222
	v_add_u32_e32 v224, 0x20000, v222
	global_load_dwordx4 v[150:153], v222, s[98:99] offset:0
	global_load_dwordx4 v[154:157], v222, s[100:101] offset:0
	global_load_dwordx4 v[158:161], v223, s[98:99] offset:0
	global_load_dwordx4 v[162:165], v223, s[100:101] offset:0
	global_load_dwordx4 v[166:169], v224, s[98:99] offset:0
	global_load_dwordx4 v[170:173], v224, s[100:101] offset:0
	global_load_dwordx4 v[174:177], v222, s[98:99] offset:64
	global_load_dwordx4 v[178:181], v222, s[100:101] offset:64
	global_load_dwordx4 v[182:185], v223, s[98:99] offset:64
	global_load_dwordx4 v[186:189], v223, s[100:101] offset:64
	global_load_dwordx4 v[190:193], v224, s[98:99] offset:64
	global_load_dwordx4 v[194:197], v224, s[100:101] offset:64
	s_waitcnt lgkmcnt(0)
	s_barrier
	v_mov_b32_e32 v3, v245
	v_xor_b32_e32 v4, v3, v1
	v_xor_b32_e32 v3, v3, v238
	v_lshl_add_u32 v4, v4, 4, v233
	v_lshl_add_u32 v3, v3, 4, v239
	v_add_u32_e32 v5, s56, v4
	v_add_u32_e32 v115, s56, v3
	ds_read_b128 v[34:37], v4
	ds_read_b128 v[30:33], v5
	ds_read_b128 v[42:45], v3
	ds_read_b128 v[38:41], v115
	global_load_dwordx4 v[198:201], v222, s[98:99] offset:128
	global_load_dwordx4 v[202:205], v222, s[100:101] offset:128
	global_load_dwordx4 v[206:209], v223, s[98:99] offset:128
	global_load_dwordx4 v[210:213], v223, s[100:101] offset:128
	global_load_dwordx4 v[214:217], v224, s[98:99] offset:128
	global_load_dwordx4 v[218:221], v224, s[100:101] offset:128
	v_add_u32_e32 v3, 4, v245
	v_xor_b32_e32 v4, v3, v1
	v_xor_b32_e32 v3, v3, v238
	v_lshl_add_u32 v4, v4, 4, v233
	v_lshl_add_u32 v3, v3, 4, v239
	v_add_u32_e32 v5, s56, v4
	v_add_u32_e32 v115, s56, v3
	ds_read_b128 v[110:113], v4
	ds_read_b128 v[116:119], v5
	ds_read_b128 v[120:123], v3
	ds_read_b128 v[124:127], v115
	s_waitcnt vmcnt(12) lgkmcnt(4)
	v_mfma_f32_16x16x32_bf16 v[26:29], v[150:153], v[34:37], v[26:29]
	v_mfma_f32_16x16x32_bf16 v[14:17], v[150:153], v[42:45], v[14:17]
	v_mfma_f32_16x16x32_bf16 v[26:29], v[154:157], v[34:37], v[26:29]
	v_mfma_f32_16x16x32_bf16 v[14:17], v[154:157], v[42:45], v[14:17]
	v_mfma_f32_16x16x32_bf16 v[26:29], v[150:153], v[30:33], v[26:29]
	v_mfma_f32_16x16x32_bf16 v[14:17], v[150:153], v[38:41], v[14:17]
	v_mfma_f32_16x16x32_bf16 v[22:25], v[158:161], v[34:37], v[22:25]
	v_mfma_f32_16x16x32_bf16 v[10:13], v[158:161], v[42:45], v[10:13]
	v_mfma_f32_16x16x32_bf16 v[22:25], v[162:165], v[34:37], v[22:25]
	v_mfma_f32_16x16x32_bf16 v[10:13], v[162:165], v[42:45], v[10:13]
	v_mfma_f32_16x16x32_bf16 v[22:25], v[158:161], v[30:33], v[22:25]
	v_mfma_f32_16x16x32_bf16 v[10:13], v[158:161], v[38:41], v[10:13]
	s_and_b64 vcc, exec, s[8:9]
	s_cbranch_vccz .Lrg_skip_0
	v_mfma_f32_16x16x32_bf16 v[18:21], v[166:169], v[34:37], v[18:21]
	v_mfma_f32_16x16x32_bf16 v[6:9], v[166:169], v[42:45], v[6:9]
	v_mfma_f32_16x16x32_bf16 v[18:21], v[170:173], v[34:37], v[18:21]
	v_mfma_f32_16x16x32_bf16 v[6:9], v[170:173], v[42:45], v[6:9]
	v_mfma_f32_16x16x32_bf16 v[18:21], v[166:169], v[30:33], v[18:21]
	v_mfma_f32_16x16x32_bf16 v[6:9], v[166:169], v[38:41], v[6:9]

.Lrg_skip_7:
.LBB0_897:
	v_mov_b32_e32 v3, v232
	s_waitcnt lgkmcnt(0)
	s_barrier
	v_mov_b32_e32 v3, v232
	v_xor_b32_e32 v4, v3, v129
	v_lshl_add_u32 v4, v4, 4, v240
	v_add_u32_e32 v5, s56, v4
	ds_write_b64 v4, v[46:47]
	ds_write_b64 v5, v[48:49]
	v_xor_b32_e32 v4, v3, v235
	v_lshl_add_u32 v4, v4, 4, v241
	v_add_u32_e32 v5, s56, v4
	ds_write_b64 v4, v[62:63]
	ds_write_b64 v5, v[64:65]
	v_xor_b32_e32 v4, v3, v236
	v_lshl_add_u32 v4, v4, 4, v242
	v_add_u32_e32 v5, s56, v4
	ds_write_b64 v4, v[78:79]
	ds_write_b64 v5, v[80:81]
	v_xor_b32_e32 v4, v3, v237
	v_lshl_add_u32 v4, v4, 4, v243
	v_add_u32_e32 v5, s56, v4
	ds_write_b64 v4, v[94:95]
	ds_write_b64 v5, v[96:97]
	v_add_u32_e32 v3, 32, v232
	v_xor_b32_e32 v4, v3, v129
	v_lshl_add_u32 v4, v4, 4, v240
	v_add_u32_e32 v5, s56, v4
	ds_write_b64 v4, v[50:51]
	ds_write_b64 v5, v[52:53]
	v_xor_b32_e32 v4, v3, v235
	v_lshl_add_u32 v4, v4, 4, v241
	v_add_u32_e32 v5, s56, v4
	ds_write_b64 v4, v[66:67]
	ds_write_b64 v5, v[68:69]
	v_xor_b32_e32 v4, v3, v236
	v_lshl_add_u32 v4, v4, 4, v242
	v_add_u32_e32 v5, s56, v4
	ds_write_b64 v4, v[82:83]
	ds_write_b64 v5, v[84:85]
	v_xor_b32_e32 v4, v3, v237
	v_lshl_add_u32 v4, v4, 4, v243
	v_add_u32_e32 v5, s56, v4
	ds_write_b64 v4, v[98:99]
	ds_write_b64 v5, v[100:101]
	v_add_u32_e32 v3, 64, v232
	v_xor_b32_e32 v4, v3, v129
	v_lshl_add_u32 v4, v4, 4, v240
	v_add_u32_e32 v5, s56, v4
	ds_write_b64 v4, v[54:55]
	ds_write_b64 v5, v[56:57]
	v_xor_b32_e32 v4, v3, v235
	v_lshl_add_u32 v4, v4, 4, v241
	v_add_u32_e32 v5, s56, v4
	ds_write_b64 v4, v[70:71]
	ds_write_b64 v5, v[72:73]
	v_xor_b32_e32 v4, v3, v236
	v_lshl_add_u32 v4, v4, 4, v242
	v_add_u32_e32 v5, s56, v4
	ds_write_b64 v4, v[86:87]
	ds_write_b64 v5, v[88:89]
	v_xor_b32_e32 v4, v3, v237
	v_lshl_add_u32 v4, v4, 4, v243
	v_add_u32_e32 v5, s56, v4
	ds_write_b64 v4, v[102:103]
	ds_write_b64 v5, v[104:105]
	v_add_u32_e32 v3, 96, v232
	v_xor_b32_e32 v4, v3, v129
	v_lshl_add_u32 v4, v4, 4, v240
	v_add_u32_e32 v5, s56, v4
	ds_write_b64 v4, v[58:59]
	ds_write_b64 v5, v[60:61]
	v_xor_b32_e32 v4, v3, v235
	v_lshl_add_u32 v4, v4, 4, v241
	v_add_u32_e32 v5, s56, v4
	ds_write_b64 v4, v[74:75]
	ds_write_b64 v5, v[76:77]
	v_xor_b32_e32 v4, v3, v236
	v_lshl_add_u32 v4, v4, 4, v242
	v_add_u32_e32 v5, s56, v4
	ds_write_b64 v4, v[90:91]
	ds_write_b64 v5, v[92:93]
	v_xor_b32_e32 v4, v3, v237
	v_lshl_add_u32 v4, v4, 4, v243
	v_add_u32_e32 v5, s56, v4
	ds_write_b64 v4, v[106:107]
	ds_write_b64 v5, v[108:109]
	s_waitcnt lgkmcnt(0)
	s_barrier
	v_mov_b32_e32 v3, v245
	v_xor_b32_e32 v4, v3, v1
	v_xor_b32_e32 v3, v3, v238
	v_lshl_add_u32 v4, v4, 4, v233
	v_lshl_add_u32 v3, v3, 4, v239
	v_add_u32_e32 v5, s56, v4
	v_add_u32_e32 v115, s56, v3
	ds_read_b128 v[34:37], v4
	ds_read_b128 v[30:33], v5
	ds_read_b128 v[42:45], v3
	ds_read_b128 v[38:41], v115
	global_load_dwordx4 v[174:177], v222, s[98:99] offset:2176
	global_load_dwordx4 v[178:181], v222, s[100:101] offset:2176
	global_load_dwordx4 v[182:185], v223, s[98:99] offset:2176
	global_load_dwordx4 v[186:189], v223, s[100:101] offset:2176
	global_load_dwordx4 v[190:193], v224, s[98:99] offset:2176
	global_load_dwordx4 v[194:197], v224, s[100:101] offset:2176
	v_add_u32_e32 v3, 4, v245
	v_xor_b32_e32 v4, v3, v1
	v_xor_b32_e32 v3, v3, v238
	v_lshl_add_u32 v4, v4, 4, v233
	v_lshl_add_u32 v3, v3, 4, v239
	v_add_u32_e32 v5, s56, v4
	v_add_u32_e32 v115, s56, v3
	ds_read_b128 v[110:113], v4
	ds_read_b128 v[116:119], v5
	ds_read_b128 v[120:123], v3
	ds_read_b128 v[124:127], v115
	s_waitcnt vmcnt(12) lgkmcnt(4)
	v_mfma_f32_16x16x32_bf16 v[26:29], v[198:201], v[34:37], v[26:29]
	v_mfma_f32_16x16x32_bf16 v[14:17], v[198:201], v[42:45], v[14:17]
	v_mfma_f32_16x16x32_bf16 v[26:29], v[202:205], v[34:37], v[26:29]
	v_mfma_f32_16x16x32_bf16 v[14:17], v[202:205], v[42:45], v[14:17]
	v_mfma_f32_16x16x32_bf16 v[26:29], v[198:201], v[30:33], v[26:29]
	v_mfma_f32_16x16x32_bf16 v[14:17], v[198:201], v[38:41], v[14:17]
	v_mfma_f32_16x16x32_bf16 v[22:25], v[206:209], v[34:37], v[22:25]
	v_mfma_f32_16x16x32_bf16 v[10:13], v[206:209], v[42:45], v[10:13]
	v_mfma_f32_16x16x32_bf16 v[22:25], v[210:213], v[34:37], v[22:25]
	v_mfma_f32_16x16x32_bf16 v[10:13], v[210:213], v[42:45], v[10:13]
	v_mfma_f32_16x16x32_bf16 v[22:25], v[206:209], v[30:33], v[22:25]
	v_mfma_f32_16x16x32_bf16 v[10:13], v[206:209], v[38:41], v[10:13]
	s_and_b64 vcc, exec, s[8:9]
	s_cbranch_vccz .Lrg_skip_8
	v_mfma_f32_16x16x32_bf16 v[18:21], v[214:217], v[34:37], v[18:21]
	v_mfma_f32_16x16x32_bf16 v[6:9], v[214:217], v[42:45], v[6:9]
	v_mfma_f32_16x16x32_bf16 v[18:21], v[218:221], v[34:37], v[18:21]
	v_mfma_f32_16x16x32_bf16 v[6:9], v[218:221], v[42:45], v[6:9]
	v_mfma_f32_16x16x32_bf16 v[18:21], v[214:217], v[30:33], v[18:21]
	v_mfma_f32_16x16x32_bf16 v[6:9], v[214:217], v[38:41], v[6:9]
